# final_d with plain (not nt) stores in the barrier-hosted tile conversion
# baseline (speedup 1.0000x reference)
.Lhw_go_s0_0:
	s_add_u32 s100, s82, s69
	s_addc_u32 s101, s83, 0
	v_readlane_b32 s82, v239, 44
	v_readlane_b32 s83, v239, 45
	s_add_u32 s82, s82, s98
	s_addc_u32 s83, s83, 0
	global_load_dword v34, v178, s[100:101] nt
	s_add_u32 s100, s100, s89
	s_addc_u32 s101, s101, 0
	global_load_dword v35, v178, s[100:101] nt
	s_add_u32 s100, s100, s89
	s_addc_u32 s101, s101, 0
	global_load_dword v36, v178, s[100:101] nt
	s_add_u32 s100, s100, s89
	s_addc_u32 s101, s101, 0
	global_load_dword v37, v178, s[100:101] nt
	s_add_u32 s100, s100, s89
	s_addc_u32 s101, s101, 0
	global_load_dword v38, v178, s[100:101] nt
	s_add_u32 s100, s100, s89
	s_addc_u32 s101, s101, 0
	global_load_dword v39, v178, s[100:101] nt
	s_add_u32 s100, s100, s89
	s_addc_u32 s101, s101, 0
	global_load_dword v40, v178, s[100:101] nt
	s_add_u32 s100, s100, s89
	s_addc_u32 s101, s101, 0
	global_load_dword v41, v178, s[100:101] nt
	s_add_u32 s100, s100, s89
	s_addc_u32 s101, s101, 0
	global_load_dword v42, v178, s[100:101] nt
	s_add_u32 s100, s100, s89
	s_addc_u32 s101, s101, 0
	global_load_dword v43, v178, s[100:101] nt
	s_add_u32 s100, s100, s89
	s_addc_u32 s101, s101, 0
	global_load_dword v44, v178, s[100:101] nt
	s_add_u32 s100, s100, s89
	s_addc_u32 s101, s101, 0
	global_load_dword v45, v178, s[100:101] nt
	s_add_u32 s100, s100, s89
	s_addc_u32 s101, s101, 0
	global_load_dword v46, v178, s[100:101] nt
	s_add_u32 s100, s100, s89
	s_addc_u32 s101, s101, 0
	global_load_dword v47, v178, s[100:101] nt
	s_add_u32 s100, s100, s89
	s_addc_u32 s101, s101, 0
	global_load_dword v48, v178, s[100:101] nt
	s_add_u32 s100, s100, s89
	s_addc_u32 s101, s101, 0
	global_load_dword v49, v178, s[100:101] nt
	s_add_u32 s100, s100, s89
	s_addc_u32 s101, s101, 0
	global_load_dword v50, v178, s[100:101] nt
	s_add_u32 s100, s100, s89
	s_addc_u32 s101, s101, 0
	global_load_dword v51, v178, s[100:101] nt
	s_add_u32 s100, s100, s89
	s_addc_u32 s101, s101, 0
	global_load_dword v52, v178, s[100:101] nt
	s_add_u32 s100, s100, s89
	s_addc_u32 s101, s101, 0
	global_load_dword v53, v178, s[100:101] nt
	s_add_u32 s100, s100, s89
	s_addc_u32 s101, s101, 0
	global_load_dword v54, v178, s[100:101] nt
	s_add_u32 s100, s100, s89
	s_addc_u32 s101, s101, 0
	global_load_dword v55, v178, s[100:101] nt
	s_add_u32 s100, s100, s89
	s_addc_u32 s101, s101, 0
	global_load_dword v56, v178, s[100:101] nt
	s_add_u32 s100, s100, s89
	s_addc_u32 s101, s101, 0
	global_load_dword v57, v178, s[100:101] nt
	s_add_u32 s100, s100, s89
	s_addc_u32 s101, s101, 0
	global_load_dword v58, v178, s[100:101] nt
	s_add_u32 s100, s100, s89
	s_addc_u32 s101, s101, 0
	global_load_dword v59, v178, s[100:101] nt
	s_add_u32 s100, s100, s89
	s_addc_u32 s101, s101, 0
	global_load_dword v60, v178, s[100:101] nt
	s_add_u32 s100, s100, s89
	s_addc_u32 s101, s101, 0
	global_load_dword v61, v178, s[100:101] nt
	s_add_u32 s100, s100, s89
	s_addc_u32 s101, s101, 0
	global_load_dword v62, v178, s[100:101] nt
	s_add_u32 s100, s100, s89
	s_addc_u32 s101, s101, 0
	global_load_dword v63, v178, s[100:101] nt
	s_add_u32 s100, s100, s89
	s_addc_u32 s101, s101, 0
	global_load_dword v64, v178, s[100:101] nt
	s_add_u32 s100, s100, s89
	s_addc_u32 s101, s101, 0
	global_load_dword v65, v178, s[100:101] nt
	s_add_u32 s100, s100, s89
	s_addc_u32 s101, s101, 0
	global_load_dword v66, v178, s[100:101] nt
	s_add_u32 s100, s100, s89
	s_addc_u32 s101, s101, 0
	global_load_dword v67, v178, s[100:101] nt
	s_add_u32 s100, s100, s89
	s_addc_u32 s101, s101, 0
	global_load_dword v68, v178, s[100:101] nt
	s_add_u32 s100, s100, s89
	s_addc_u32 s101, s101, 0
	global_load_dword v69, v178, s[100:101] nt
	s_add_u32 s100, s100, s89
	s_addc_u32 s101, s101, 0
	global_load_dword v70, v178, s[100:101] nt
	s_add_u32 s100, s100, s89
	s_addc_u32 s101, s101, 0
	global_load_dword v71, v178, s[100:101] nt
	s_add_u32 s100, s100, s89
	s_addc_u32 s101, s101, 0
	global_load_dword v72, v178, s[100:101] nt
	s_add_u32 s100, s100, s89
	s_addc_u32 s101, s101, 0
	global_load_dword v73, v178, s[100:101] nt
	s_add_u32 s100, s100, s89
	s_addc_u32 s101, s101, 0
	global_load_dword v74, v178, s[100:101] nt
	s_add_u32 s100, s100, s89
	s_addc_u32 s101, s101, 0
	global_load_dword v75, v178, s[100:101] nt
	s_add_u32 s100, s100, s89
	s_addc_u32 s101, s101, 0
	global_load_dword v76, v178, s[100:101] nt
	s_add_u32 s100, s100, s89
	s_addc_u32 s101, s101, 0
	global_load_dword v77, v178, s[100:101] nt
	s_add_u32 s100, s100, s89
	s_addc_u32 s101, s101, 0
	global_load_dword v78, v178, s[100:101] nt
	s_add_u32 s100, s100, s89
	s_addc_u32 s101, s101, 0
	global_load_dword v79, v178, s[100:101] nt
	s_add_u32 s100, s100, s89
	s_addc_u32 s101, s101, 0
	global_load_dword v80, v178, s[100:101] nt
	s_add_u32 s100, s100, s89
	s_addc_u32 s101, s101, 0
	global_load_dword v81, v178, s[100:101] nt
	s_add_u32 s100, s100, s89
	s_addc_u32 s101, s101, 0
	global_load_dword v82, v178, s[100:101] nt
	s_add_u32 s100, s100, s89
	s_addc_u32 s101, s101, 0
	global_load_dword v83, v178, s[100:101] nt
	s_add_u32 s100, s100, s89
	s_addc_u32 s101, s101, 0
	global_load_dword v84, v178, s[100:101] nt
	s_add_u32 s100, s100, s89
	s_addc_u32 s101, s101, 0
	global_load_dword v85, v178, s[100:101] nt
	s_add_u32 s100, s100, s89
	s_addc_u32 s101, s101, 0
	global_load_dword v86, v178, s[100:101] nt
	s_add_u32 s100, s100, s89
	s_addc_u32 s101, s101, 0
	global_load_dword v87, v178, s[100:101] nt
	s_add_u32 s100, s100, s89
	s_addc_u32 s101, s101, 0
	global_load_dword v88, v178, s[100:101] nt
	s_add_u32 s100, s100, s89
	s_addc_u32 s101, s101, 0
	global_load_dword v89, v178, s[100:101] nt
	s_add_u32 s100, s100, s89
	s_addc_u32 s101, s101, 0
	global_load_dword v90, v178, s[100:101] nt
	s_add_u32 s100, s100, s89
	s_addc_u32 s101, s101, 0
	global_load_dword v91, v178, s[100:101] nt
	s_add_u32 s100, s100, s89
	s_addc_u32 s101, s101, 0
	global_load_dword v92, v178, s[100:101] nt
	s_add_u32 s100, s100, s89
	s_addc_u32 s101, s101, 0
	global_load_dword v93, v178, s[100:101] nt
	s_add_u32 s100, s100, s89
	s_addc_u32 s101, s101, 0
	global_load_dword v94, v178, s[100:101] nt
	s_add_u32 s100, s100, s89
	s_addc_u32 s101, s101, 0
	global_load_dword v95, v178, s[100:101] nt
	s_add_u32 s100, s100, s89
	s_addc_u32 s101, s101, 0
	global_load_dword v96, v178, s[100:101] nt
	s_add_u32 s100, s100, s89
	s_addc_u32 s101, s101, 0
	global_load_dword v97, v178, s[100:101] nt
	s_add_u32 s100, s100, s89
	s_addc_u32 s101, s101, 0
	s_waitcnt vmcnt(48)
	v_mul_f32_e32 v34, 0x42000000, v34
	v_mul_f32_e32 v35, 0x42000000, v35
	v_mul_f32_e32 v36, 0x42000000, v36
	v_mul_f32_e32 v37, 0x42000000, v37
	v_mul_f32_e32 v38, 0x42000000, v38
	v_mul_f32_e32 v39, 0x42000000, v39
	v_mul_f32_e32 v40, 0x42000000, v40
	v_mul_f32_e32 v41, 0x42000000, v41
	v_mul_f32_e32 v42, 0x42000000, v42
	v_mul_f32_e32 v43, 0x42000000, v43
	v_mul_f32_e32 v44, 0x42000000, v44
	v_mul_f32_e32 v45, 0x42000000, v45
	v_mul_f32_e32 v46, 0x42000000, v46
	v_mul_f32_e32 v47, 0x42000000, v47
	v_mul_f32_e32 v48, 0x42000000, v48
	v_mul_f32_e32 v49, 0x42000000, v49
	v_cvt_pk_fp8_f32 v154, v34, v35
	v_cvt_pk_fp8_f32 v155, v38, v39
	v_cvt_pk_fp8_f32 v156, v42, v43
	v_cvt_pk_fp8_f32 v157, v46, v47
	v_cvt_pk_fp8_f32 v154, v36, v37 op_sel:[0,0,1]
	v_cvt_pk_fp8_f32 v155, v40, v41 op_sel:[0,0,1]
	v_cvt_pk_fp8_f32 v156, v44, v45 op_sel:[0,0,1]
	v_cvt_pk_fp8_f32 v157, v48, v49 op_sel:[0,0,1]
	s_waitcnt vmcnt(32)
	v_mul_f32_e32 v50, 0x42000000, v50
	v_mul_f32_e32 v51, 0x42000000, v51
	v_mul_f32_e32 v52, 0x42000000, v52
	v_mul_f32_e32 v53, 0x42000000, v53
	v_mul_f32_e32 v54, 0x42000000, v54
	v_mul_f32_e32 v55, 0x42000000, v55
	v_mul_f32_e32 v56, 0x42000000, v56
	v_mul_f32_e32 v57, 0x42000000, v57
	v_mul_f32_e32 v58, 0x42000000, v58
	v_mul_f32_e32 v59, 0x42000000, v59
	v_mul_f32_e32 v60, 0x42000000, v60
	v_mul_f32_e32 v61, 0x42000000, v61
	v_mul_f32_e32 v62, 0x42000000, v62
	v_mul_f32_e32 v63, 0x42000000, v63
	v_mul_f32_e32 v64, 0x42000000, v64
	v_mul_f32_e32 v65, 0x42000000, v65
	v_cvt_pk_fp8_f32 v158, v50, v51
	v_cvt_pk_fp8_f32 v159, v54, v55
	v_cvt_pk_fp8_f32 v160, v58, v59
	v_cvt_pk_fp8_f32 v161, v62, v63
	v_cvt_pk_fp8_f32 v158, v52, v53 op_sel:[0,0,1]
	v_cvt_pk_fp8_f32 v159, v56, v57 op_sel:[0,0,1]
	v_cvt_pk_fp8_f32 v160, v60, v61 op_sel:[0,0,1]
	v_cvt_pk_fp8_f32 v161, v64, v65 op_sel:[0,0,1]
	s_waitcnt vmcnt(16)
	v_mul_f32_e32 v66, 0x42000000, v66
	v_mul_f32_e32 v67, 0x42000000, v67
	v_mul_f32_e32 v68, 0x42000000, v68
	v_mul_f32_e32 v69, 0x42000000, v69
	v_mul_f32_e32 v70, 0x42000000, v70
	v_mul_f32_e32 v71, 0x42000000, v71
	v_mul_f32_e32 v72, 0x42000000, v72
	v_mul_f32_e32 v73, 0x42000000, v73
	v_mul_f32_e32 v74, 0x42000000, v74
	v_mul_f32_e32 v75, 0x42000000, v75
	v_mul_f32_e32 v76, 0x42000000, v76
	v_mul_f32_e32 v77, 0x42000000, v77
	v_mul_f32_e32 v78, 0x42000000, v78
	v_mul_f32_e32 v79, 0x42000000, v79
	v_mul_f32_e32 v80, 0x42000000, v80
	v_mul_f32_e32 v81, 0x42000000, v81
	v_cvt_pk_fp8_f32 v162, v66, v67
	v_cvt_pk_fp8_f32 v163, v70, v71
	v_cvt_pk_fp8_f32 v164, v74, v75
	v_cvt_pk_fp8_f32 v165, v78, v79
	v_cvt_pk_fp8_f32 v162, v68, v69 op_sel:[0,0,1]
	v_cvt_pk_fp8_f32 v163, v72, v73 op_sel:[0,0,1]
	v_cvt_pk_fp8_f32 v164, v76, v77 op_sel:[0,0,1]
	v_cvt_pk_fp8_f32 v165, v80, v81 op_sel:[0,0,1]
	s_waitcnt vmcnt(0)
	v_mul_f32_e32 v82, 0x42000000, v82
	v_mul_f32_e32 v83, 0x42000000, v83
	v_mul_f32_e32 v84, 0x42000000, v84
	v_mul_f32_e32 v85, 0x42000000, v85
	v_mul_f32_e32 v86, 0x42000000, v86
	v_mul_f32_e32 v87, 0x42000000, v87
	v_mul_f32_e32 v88, 0x42000000, v88
	v_mul_f32_e32 v89, 0x42000000, v89
	v_mul_f32_e32 v90, 0x42000000, v90
	v_mul_f32_e32 v91, 0x42000000, v91
	v_mul_f32_e32 v92, 0x42000000, v92
	v_mul_f32_e32 v93, 0x42000000, v93
	v_mul_f32_e32 v94, 0x42000000, v94
	v_mul_f32_e32 v95, 0x42000000, v95
	v_mul_f32_e32 v96, 0x42000000, v96
	v_mul_f32_e32 v97, 0x42000000, v97
	v_cvt_pk_fp8_f32 v166, v82, v83
	v_cvt_pk_fp8_f32 v167, v86, v87
	v_cvt_pk_fp8_f32 v168, v90, v91
	v_cvt_pk_fp8_f32 v169, v94, v95
	v_cvt_pk_fp8_f32 v166, v84, v85 op_sel:[0,0,1]
	v_cvt_pk_fp8_f32 v167, v88, v89 op_sel:[0,0,1]
	v_cvt_pk_fp8_f32 v168, v92, v93 op_sel:[0,0,1]
	v_cvt_pk_fp8_f32 v169, v96, v97 op_sel:[0,0,1]
	s_mov_b32 vcc_lo, 0xaaaaaaaa
	s_mov_b32 vcc_hi, 0xaaaaaaaa
	s_nop 1
	v_cndmask_b32_dpp v170, v154, v158, vcc quad_perm:[1,0,3,2] row_mask:0xf bank_mask:0xf
	v_cndmask_b32_dpp v174, v162, v166, vcc quad_perm:[1,0,3,2] row_mask:0xf bank_mask:0xf
	v_cndmask_b32_dpp v171, v155, v159, vcc quad_perm:[1,0,3,2] row_mask:0xf bank_mask:0xf
	v_cndmask_b32_dpp v175, v163, v167, vcc quad_perm:[1,0,3,2] row_mask:0xf bank_mask:0xf
	v_cndmask_b32_dpp v172, v156, v160, vcc quad_perm:[1,0,3,2] row_mask:0xf bank_mask:0xf
	v_cndmask_b32_dpp v176, v164, v168, vcc quad_perm:[1,0,3,2] row_mask:0xf bank_mask:0xf
	v_cndmask_b32_dpp v173, v157, v161, vcc quad_perm:[1,0,3,2] row_mask:0xf bank_mask:0xf
	v_cndmask_b32_dpp v177, v165, v169, vcc quad_perm:[1,0,3,2] row_mask:0xf bank_mask:0xf
	s_mov_b32 vcc_lo, 0x55555555
	s_mov_b32 vcc_hi, 0x55555555
	s_nop 1
	v_cndmask_b32_dpp v154, v158, v154, vcc quad_perm:[1,0,3,2] row_mask:0xf bank_mask:0xf
	v_cndmask_b32_dpp v162, v166, v162, vcc quad_perm:[1,0,3,2] row_mask:0xf bank_mask:0xf
	v_cndmask_b32_dpp v155, v159, v155, vcc quad_perm:[1,0,3,2] row_mask:0xf bank_mask:0xf
	v_cndmask_b32_dpp v163, v167, v163, vcc quad_perm:[1,0,3,2] row_mask:0xf bank_mask:0xf
	v_cndmask_b32_dpp v156, v160, v156, vcc quad_perm:[1,0,3,2] row_mask:0xf bank_mask:0xf
	v_cndmask_b32_dpp v164, v168, v164, vcc quad_perm:[1,0,3,2] row_mask:0xf bank_mask:0xf
	v_cndmask_b32_dpp v157, v161, v157, vcc quad_perm:[1,0,3,2] row_mask:0xf bank_mask:0xf
	v_cndmask_b32_dpp v165, v169, v165, vcc quad_perm:[1,0,3,2] row_mask:0xf bank_mask:0xf
	s_mov_b32 vcc_lo, 0xcccccccc
	s_mov_b32 vcc_hi, 0xcccccccc
	s_nop 1
	v_cndmask_b32_dpp v158, v154, v162, vcc quad_perm:[2,3,0,1] row_mask:0xf bank_mask:0xf
	v_cndmask_b32_dpp v166, v170, v174, vcc quad_perm:[2,3,0,1] row_mask:0xf bank_mask:0xf
	v_cndmask_b32_dpp v159, v155, v163, vcc quad_perm:[2,3,0,1] row_mask:0xf bank_mask:0xf
	v_cndmask_b32_dpp v167, v171, v175, vcc quad_perm:[2,3,0,1] row_mask:0xf bank_mask:0xf
	v_cndmask_b32_dpp v160, v156, v164, vcc quad_perm:[2,3,0,1] row_mask:0xf bank_mask:0xf
	v_cndmask_b32_dpp v168, v172, v176, vcc quad_perm:[2,3,0,1] row_mask:0xf bank_mask:0xf
	v_cndmask_b32_dpp v161, v157, v165, vcc quad_perm:[2,3,0,1] row_mask:0xf bank_mask:0xf
	v_cndmask_b32_dpp v169, v173, v177, vcc quad_perm:[2,3,0,1] row_mask:0xf bank_mask:0xf
	s_mov_b32 vcc_lo, 0x33333333
	s_mov_b32 vcc_hi, 0x33333333
	s_nop 1
	v_cndmask_b32_dpp v154, v162, v154, vcc quad_perm:[2,3,0,1] row_mask:0xf bank_mask:0xf
	v_cndmask_b32_dpp v170, v174, v170, vcc quad_perm:[2,3,0,1] row_mask:0xf bank_mask:0xf
	v_cndmask_b32_dpp v155, v163, v155, vcc quad_perm:[2,3,0,1] row_mask:0xf bank_mask:0xf
	v_cndmask_b32_dpp v171, v175, v171, vcc quad_perm:[2,3,0,1] row_mask:0xf bank_mask:0xf
	v_cndmask_b32_dpp v156, v164, v156, vcc quad_perm:[2,3,0,1] row_mask:0xf bank_mask:0xf
	v_cndmask_b32_dpp v172, v176, v172, vcc quad_perm:[2,3,0,1] row_mask:0xf bank_mask:0xf
	v_cndmask_b32_dpp v157, v165, v157, vcc quad_perm:[2,3,0,1] row_mask:0xf bank_mask:0xf
	v_cndmask_b32_dpp v173, v177, v173, vcc quad_perm:[2,3,0,1] row_mask:0xf bank_mask:0xf
	global_store_dwordx4 v179, v[154:157], s[82:83]
	global_store_dwordx4 v180, v[170:173], s[82:83]
	global_store_dwordx4 v181, v[158:161], s[82:83]
	global_store_dwordx4 v190, v[166:169], s[82:83]
	v_readlane_b32 s2, v239, 0
	s_lshr_b32 s2, s2, 6
	s_add_i32 s2, s2, 6
	s_cmp_gt_u32 s2, 13
	s_cbranch_scc1 .Lhw_seam0_done
	s_add_i32 s2, s2, 0
	s_mul_i32 s2, s2, s74
	v_readlane_b32 s9, v239, 23
	s_lshr_b32 s9, s9, 3
	s_add_i32 s2, s2, s9
	s_cmp_gt_u32 s2, 24575
	s_cbranch_scc1 .Lhw_seam0_done
	v_mbcnt_lo_u32_b32 v178, -1, 0
	v_mbcnt_hi_u32_b32 v178, -1, v178
	v_and_b32_e32 v179, 60, v178
	v_lshlrev_b32_e32 v179, 10, v179
	v_and_b32_e32 v180, 3, v178
	v_lshl_or_b32 v179, v180, 4, v179
	v_add_u32_e32 v180, 0x400, v179
	v_add_u32_e32 v181, 0x800, v179
	v_add_u32_e32 v190, 0xc00, v179
	v_lshlrev_b32_e32 v178, 2, v178
	s_cmp_lt_u32 s2, 16384
	s_cbranch_scc0 .Lhw_dn_s0_1
	s_lshr_b32 s9, s2, 9
	s_bfe_u32 s32, s2, 0x40005
	s_and_b32 s53, s2, 31
	s_lshl_b32 s69, s9, 23
	s_lshl_b32 s100, s32, 19
	s_add_i32 s69, s69, s100
	s_lshl_b32 s100, s53, 8
	s_add_i32 s69, s69, s100
	s_lshl_b32 s98, s9, 11
	s_bfe_u32 s100, s53, 0x30001
	s_lshl_b32 s100, s100, 8
	s_add_i32 s98, s98, s100
	s_lshr_b32 s100, s53, 4
	s_lshl_b32 s100, s100, 7
	s_add_i32 s98, s98, s100
	s_and_b32 s100, s53, 1
	s_lshl_b32 s100, s100, 6
	s_add_i32 s98, s98, s100
	s_lshl_b32 s98, s98, 10
	s_lshl_b32 s100, s32, 6
	s_add_i32 s98, s98, s100
	s_add_i32 s98, s98, 0x2000000
	v_readlane_b32 s82, v239, 11
	v_readlane_b32 s83, v239, 12
	s_movk_i32 s89, 8192
	s_branch .Lhw_go_s0_1

.Lhw_go_s0_1:
	s_add_u32 s100, s82, s69
	s_addc_u32 s101, s83, 0
	v_readlane_b32 s82, v239, 44
	v_readlane_b32 s83, v239, 45
	s_add_u32 s82, s82, s98
	s_addc_u32 s83, s83, 0
	global_load_dword v34, v178, s[100:101] nt
	s_add_u32 s100, s100, s89
	s_addc_u32 s101, s101, 0
	global_load_dword v35, v178, s[100:101] nt
	s_add_u32 s100, s100, s89
	s_addc_u32 s101, s101, 0
	global_load_dword v36, v178, s[100:101] nt
	s_add_u32 s100, s100, s89
	s_addc_u32 s101, s101, 0
	global_load_dword v37, v178, s[100:101] nt
	s_add_u32 s100, s100, s89
	s_addc_u32 s101, s101, 0
	global_load_dword v38, v178, s[100:101] nt
	s_add_u32 s100, s100, s89
	s_addc_u32 s101, s101, 0
	global_load_dword v39, v178, s[100:101] nt
	s_add_u32 s100, s100, s89
	s_addc_u32 s101, s101, 0
	global_load_dword v40, v178, s[100:101] nt
	s_add_u32 s100, s100, s89
	s_addc_u32 s101, s101, 0
	global_load_dword v41, v178, s[100:101] nt
	s_add_u32 s100, s100, s89
	s_addc_u32 s101, s101, 0
	global_load_dword v42, v178, s[100:101] nt
	s_add_u32 s100, s100, s89
	s_addc_u32 s101, s101, 0
	global_load_dword v43, v178, s[100:101] nt
	s_add_u32 s100, s100, s89
	s_addc_u32 s101, s101, 0
	global_load_dword v44, v178, s[100:101] nt
	s_add_u32 s100, s100, s89
	s_addc_u32 s101, s101, 0
	global_load_dword v45, v178, s[100:101] nt
	s_add_u32 s100, s100, s89
	s_addc_u32 s101, s101, 0
	global_load_dword v46, v178, s[100:101] nt
	s_add_u32 s100, s100, s89
	s_addc_u32 s101, s101, 0
	global_load_dword v47, v178, s[100:101] nt
	s_add_u32 s100, s100, s89
	s_addc_u32 s101, s101, 0
	global_load_dword v48, v178, s[100:101] nt
	s_add_u32 s100, s100, s89
	s_addc_u32 s101, s101, 0
	global_load_dword v49, v178, s[100:101] nt
	s_add_u32 s100, s100, s89
	s_addc_u32 s101, s101, 0
	global_load_dword v50, v178, s[100:101] nt
	s_add_u32 s100, s100, s89
	s_addc_u32 s101, s101, 0
	global_load_dword v51, v178, s[100:101] nt
	s_add_u32 s100, s100, s89
	s_addc_u32 s101, s101, 0
	global_load_dword v52, v178, s[100:101] nt
	s_add_u32 s100, s100, s89
	s_addc_u32 s101, s101, 0
	global_load_dword v53, v178, s[100:101] nt
	s_add_u32 s100, s100, s89
	s_addc_u32 s101, s101, 0
	global_load_dword v54, v178, s[100:101] nt
	s_add_u32 s100, s100, s89
	s_addc_u32 s101, s101, 0
	global_load_dword v55, v178, s[100:101] nt
	s_add_u32 s100, s100, s89
	s_addc_u32 s101, s101, 0
	global_load_dword v56, v178, s[100:101] nt
	s_add_u32 s100, s100, s89
	s_addc_u32 s101, s101, 0
	global_load_dword v57, v178, s[100:101] nt
	s_add_u32 s100, s100, s89
	s_addc_u32 s101, s101, 0
	global_load_dword v58, v178, s[100:101] nt
	s_add_u32 s100, s100, s89
	s_addc_u32 s101, s101, 0
	global_load_dword v59, v178, s[100:101] nt
	s_add_u32 s100, s100, s89
	s_addc_u32 s101, s101, 0
	global_load_dword v60, v178, s[100:101] nt
	s_add_u32 s100, s100, s89
	s_addc_u32 s101, s101, 0
	global_load_dword v61, v178, s[100:101] nt
	s_add_u32 s100, s100, s89
	s_addc_u32 s101, s101, 0
	global_load_dword v62, v178, s[100:101] nt
	s_add_u32 s100, s100, s89
	s_addc_u32 s101, s101, 0
	global_load_dword v63, v178, s[100:101] nt
	s_add_u32 s100, s100, s89
	s_addc_u32 s101, s101, 0
	global_load_dword v64, v178, s[100:101] nt
	s_add_u32 s100, s100, s89
	s_addc_u32 s101, s101, 0
	global_load_dword v65, v178, s[100:101] nt
	s_add_u32 s100, s100, s89
	s_addc_u32 s101, s101, 0
	global_load_dword v66, v178, s[100:101] nt
	s_add_u32 s100, s100, s89
	s_addc_u32 s101, s101, 0
	global_load_dword v67, v178, s[100:101] nt
	s_add_u32 s100, s100, s89
	s_addc_u32 s101, s101, 0
	global_load_dword v68, v178, s[100:101] nt
	s_add_u32 s100, s100, s89
	s_addc_u32 s101, s101, 0
	global_load_dword v69, v178, s[100:101] nt
	s_add_u32 s100, s100, s89
	s_addc_u32 s101, s101, 0
	global_load_dword v70, v178, s[100:101] nt
	s_add_u32 s100, s100, s89
	s_addc_u32 s101, s101, 0
	global_load_dword v71, v178, s[100:101] nt
	s_add_u32 s100, s100, s89
	s_addc_u32 s101, s101, 0
	global_load_dword v72, v178, s[100:101] nt
	s_add_u32 s100, s100, s89
	s_addc_u32 s101, s101, 0
	global_load_dword v73, v178, s[100:101] nt
	s_add_u32 s100, s100, s89
	s_addc_u32 s101, s101, 0
	global_load_dword v74, v178, s[100:101] nt
	s_add_u32 s100, s100, s89
	s_addc_u32 s101, s101, 0
	global_load_dword v75, v178, s[100:101] nt
	s_add_u32 s100, s100, s89
	s_addc_u32 s101, s101, 0
	global_load_dword v76, v178, s[100:101] nt
	s_add_u32 s100, s100, s89
	s_addc_u32 s101, s101, 0
	global_load_dword v77, v178, s[100:101] nt
	s_add_u32 s100, s100, s89
	s_addc_u32 s101, s101, 0
	global_load_dword v78, v178, s[100:101] nt
	s_add_u32 s100, s100, s89
	s_addc_u32 s101, s101, 0
	global_load_dword v79, v178, s[100:101] nt
	s_add_u32 s100, s100, s89
	s_addc_u32 s101, s101, 0
	global_load_dword v80, v178, s[100:101] nt
	s_add_u32 s100, s100, s89
	s_addc_u32 s101, s101, 0
	global_load_dword v81, v178, s[100:101] nt
	s_add_u32 s100, s100, s89
	s_addc_u32 s101, s101, 0
	global_load_dword v82, v178, s[100:101] nt
	s_add_u32 s100, s100, s89
	s_addc_u32 s101, s101, 0
	global_load_dword v83, v178, s[100:101] nt
	s_add_u32 s100, s100, s89
	s_addc_u32 s101, s101, 0
	global_load_dword v84, v178, s[100:101] nt
	s_add_u32 s100, s100, s89
	s_addc_u32 s101, s101, 0
	global_load_dword v85, v178, s[100:101] nt
	s_add_u32 s100, s100, s89
	s_addc_u32 s101, s101, 0
	global_load_dword v86, v178, s[100:101] nt
	s_add_u32 s100, s100, s89
	s_addc_u32 s101, s101, 0
	global_load_dword v87, v178, s[100:101] nt
	s_add_u32 s100, s100, s89
	s_addc_u32 s101, s101, 0
	global_load_dword v88, v178, s[100:101] nt
	s_add_u32 s100, s100, s89
	s_addc_u32 s101, s101, 0
	global_load_dword v89, v178, s[100:101] nt
	s_add_u32 s100, s100, s89
	s_addc_u32 s101, s101, 0
	global_load_dword v90, v178, s[100:101] nt
	s_add_u32 s100, s100, s89
	s_addc_u32 s101, s101, 0
	global_load_dword v91, v178, s[100:101] nt
	s_add_u32 s100, s100, s89
	s_addc_u32 s101, s101, 0
	global_load_dword v92, v178, s[100:101] nt
	s_add_u32 s100, s100, s89
	s_addc_u32 s101, s101, 0
	global_load_dword v93, v178, s[100:101] nt
	s_add_u32 s100, s100, s89
	s_addc_u32 s101, s101, 0
	global_load_dword v94, v178, s[100:101] nt
	s_add_u32 s100, s100, s89
	s_addc_u32 s101, s101, 0
	global_load_dword v95, v178, s[100:101] nt
	s_add_u32 s100, s100, s89
	s_addc_u32 s101, s101, 0
	global_load_dword v96, v178, s[100:101] nt
	s_add_u32 s100, s100, s89
	s_addc_u32 s101, s101, 0
	global_load_dword v97, v178, s[100:101] nt
	s_add_u32 s100, s100, s89
	s_addc_u32 s101, s101, 0
	s_waitcnt vmcnt(48)
	v_mul_f32_e32 v34, 0x42000000, v34
	v_mul_f32_e32 v35, 0x42000000, v35
	v_mul_f32_e32 v36, 0x42000000, v36
	v_mul_f32_e32 v37, 0x42000000, v37
	v_mul_f32_e32 v38, 0x42000000, v38
	v_mul_f32_e32 v39, 0x42000000, v39
	v_mul_f32_e32 v40, 0x42000000, v40
	v_mul_f32_e32 v41, 0x42000000, v41
	v_mul_f32_e32 v42, 0x42000000, v42
	v_mul_f32_e32 v43, 0x42000000, v43
	v_mul_f32_e32 v44, 0x42000000, v44
	v_mul_f32_e32 v45, 0x42000000, v45
	v_mul_f32_e32 v46, 0x42000000, v46
	v_mul_f32_e32 v47, 0x42000000, v47
	v_mul_f32_e32 v48, 0x42000000, v48
	v_mul_f32_e32 v49, 0x42000000, v49
	v_cvt_pk_fp8_f32 v154, v34, v35
	v_cvt_pk_fp8_f32 v155, v38, v39
	v_cvt_pk_fp8_f32 v156, v42, v43
	v_cvt_pk_fp8_f32 v157, v46, v47
	v_cvt_pk_fp8_f32 v154, v36, v37 op_sel:[0,0,1]
	v_cvt_pk_fp8_f32 v155, v40, v41 op_sel:[0,0,1]
	v_cvt_pk_fp8_f32 v156, v44, v45 op_sel:[0,0,1]
	v_cvt_pk_fp8_f32 v157, v48, v49 op_sel:[0,0,1]
	s_waitcnt vmcnt(32)
	v_mul_f32_e32 v50, 0x42000000, v50
	v_mul_f32_e32 v51, 0x42000000, v51
	v_mul_f32_e32 v52, 0x42000000, v52
	v_mul_f32_e32 v53, 0x42000000, v53
	v_mul_f32_e32 v54, 0x42000000, v54
	v_mul_f32_e32 v55, 0x42000000, v55
	v_mul_f32_e32 v56, 0x42000000, v56
	v_mul_f32_e32 v57, 0x42000000, v57
	v_mul_f32_e32 v58, 0x42000000, v58
	v_mul_f32_e32 v59, 0x42000000, v59
	v_mul_f32_e32 v60, 0x42000000, v60
	v_mul_f32_e32 v61, 0x42000000, v61
	v_mul_f32_e32 v62, 0x42000000, v62
	v_mul_f32_e32 v63, 0x42000000, v63
	v_mul_f32_e32 v64, 0x42000000, v64
	v_mul_f32_e32 v65, 0x42000000, v65
	v_cvt_pk_fp8_f32 v158, v50, v51
	v_cvt_pk_fp8_f32 v159, v54, v55
	v_cvt_pk_fp8_f32 v160, v58, v59
	v_cvt_pk_fp8_f32 v161, v62, v63
	v_cvt_pk_fp8_f32 v158, v52, v53 op_sel:[0,0,1]
	v_cvt_pk_fp8_f32 v159, v56, v57 op_sel:[0,0,1]
	v_cvt_pk_fp8_f32 v160, v60, v61 op_sel:[0,0,1]
	v_cvt_pk_fp8_f32 v161, v64, v65 op_sel:[0,0,1]
	s_waitcnt vmcnt(16)
	v_mul_f32_e32 v66, 0x42000000, v66
	v_mul_f32_e32 v67, 0x42000000, v67
	v_mul_f32_e32 v68, 0x42000000, v68
	v_mul_f32_e32 v69, 0x42000000, v69
	v_mul_f32_e32 v70, 0x42000000, v70
	v_mul_f32_e32 v71, 0x42000000, v71
	v_mul_f32_e32 v72, 0x42000000, v72
	v_mul_f32_e32 v73, 0x42000000, v73
	v_mul_f32_e32 v74, 0x42000000, v74
	v_mul_f32_e32 v75, 0x42000000, v75
	v_mul_f32_e32 v76, 0x42000000, v76
	v_mul_f32_e32 v77, 0x42000000, v77
	v_mul_f32_e32 v78, 0x42000000, v78
	v_mul_f32_e32 v79, 0x42000000, v79
	v_mul_f32_e32 v80, 0x42000000, v80
	v_mul_f32_e32 v81, 0x42000000, v81
	v_cvt_pk_fp8_f32 v162, v66, v67
	v_cvt_pk_fp8_f32 v163, v70, v71
	v_cvt_pk_fp8_f32 v164, v74, v75
	v_cvt_pk_fp8_f32 v165, v78, v79
	v_cvt_pk_fp8_f32 v162, v68, v69 op_sel:[0,0,1]
	v_cvt_pk_fp8_f32 v163, v72, v73 op_sel:[0,0,1]
	v_cvt_pk_fp8_f32 v164, v76, v77 op_sel:[0,0,1]
	v_cvt_pk_fp8_f32 v165, v80, v81 op_sel:[0,0,1]
	s_waitcnt vmcnt(0)
	v_mul_f32_e32 v82, 0x42000000, v82
	v_mul_f32_e32 v83, 0x42000000, v83
	v_mul_f32_e32 v84, 0x42000000, v84
	v_mul_f32_e32 v85, 0x42000000, v85
	v_mul_f32_e32 v86, 0x42000000, v86
	v_mul_f32_e32 v87, 0x42000000, v87
	v_mul_f32_e32 v88, 0x42000000, v88
	v_mul_f32_e32 v89, 0x42000000, v89
	v_mul_f32_e32 v90, 0x42000000, v90
	v_mul_f32_e32 v91, 0x42000000, v91
	v_mul_f32_e32 v92, 0x42000000, v92
	v_mul_f32_e32 v93, 0x42000000, v93
	v_mul_f32_e32 v94, 0x42000000, v94
	v_mul_f32_e32 v95, 0x42000000, v95
	v_mul_f32_e32 v96, 0x42000000, v96
	v_mul_f32_e32 v97, 0x42000000, v97
	v_cvt_pk_fp8_f32 v166, v82, v83
	v_cvt_pk_fp8_f32 v167, v86, v87
	v_cvt_pk_fp8_f32 v168, v90, v91
	v_cvt_pk_fp8_f32 v169, v94, v95
	v_cvt_pk_fp8_f32 v166, v84, v85 op_sel:[0,0,1]
	v_cvt_pk_fp8_f32 v167, v88, v89 op_sel:[0,0,1]
	v_cvt_pk_fp8_f32 v168, v92, v93 op_sel:[0,0,1]
	v_cvt_pk_fp8_f32 v169, v96, v97 op_sel:[0,0,1]
	s_mov_b32 vcc_lo, 0xaaaaaaaa
	s_mov_b32 vcc_hi, 0xaaaaaaaa
	s_nop 1
	v_cndmask_b32_dpp v170, v154, v158, vcc quad_perm:[1,0,3,2] row_mask:0xf bank_mask:0xf
	v_cndmask_b32_dpp v174, v162, v166, vcc quad_perm:[1,0,3,2] row_mask:0xf bank_mask:0xf
	v_cndmask_b32_dpp v171, v155, v159, vcc quad_perm:[1,0,3,2] row_mask:0xf bank_mask:0xf
	v_cndmask_b32_dpp v175, v163, v167, vcc quad_perm:[1,0,3,2] row_mask:0xf bank_mask:0xf
	v_cndmask_b32_dpp v172, v156, v160, vcc quad_perm:[1,0,3,2] row_mask:0xf bank_mask:0xf
	v_cndmask_b32_dpp v176, v164, v168, vcc quad_perm:[1,0,3,2] row_mask:0xf bank_mask:0xf
	v_cndmask_b32_dpp v173, v157, v161, vcc quad_perm:[1,0,3,2] row_mask:0xf bank_mask:0xf
	v_cndmask_b32_dpp v177, v165, v169, vcc quad_perm:[1,0,3,2] row_mask:0xf bank_mask:0xf
	s_mov_b32 vcc_lo, 0x55555555
	s_mov_b32 vcc_hi, 0x55555555
	s_nop 1
	v_cndmask_b32_dpp v154, v158, v154, vcc quad_perm:[1,0,3,2] row_mask:0xf bank_mask:0xf
	v_cndmask_b32_dpp v162, v166, v162, vcc quad_perm:[1,0,3,2] row_mask:0xf bank_mask:0xf
	v_cndmask_b32_dpp v155, v159, v155, vcc quad_perm:[1,0,3,2] row_mask:0xf bank_mask:0xf
	v_cndmask_b32_dpp v163, v167, v163, vcc quad_perm:[1,0,3,2] row_mask:0xf bank_mask:0xf
	v_cndmask_b32_dpp v156, v160, v156, vcc quad_perm:[1,0,3,2] row_mask:0xf bank_mask:0xf
	v_cndmask_b32_dpp v164, v168, v164, vcc quad_perm:[1,0,3,2] row_mask:0xf bank_mask:0xf
	v_cndmask_b32_dpp v157, v161, v157, vcc quad_perm:[1,0,3,2] row_mask:0xf bank_mask:0xf
	v_cndmask_b32_dpp v165, v169, v165, vcc quad_perm:[1,0,3,2] row_mask:0xf bank_mask:0xf
	s_mov_b32 vcc_lo, 0xcccccccc
	s_mov_b32 vcc_hi, 0xcccccccc
	s_nop 1
	v_cndmask_b32_dpp v158, v154, v162, vcc quad_perm:[2,3,0,1] row_mask:0xf bank_mask:0xf
	v_cndmask_b32_dpp v166, v170, v174, vcc quad_perm:[2,3,0,1] row_mask:0xf bank_mask:0xf
	v_cndmask_b32_dpp v159, v155, v163, vcc quad_perm:[2,3,0,1] row_mask:0xf bank_mask:0xf
	v_cndmask_b32_dpp v167, v171, v175, vcc quad_perm:[2,3,0,1] row_mask:0xf bank_mask:0xf
	v_cndmask_b32_dpp v160, v156, v164, vcc quad_perm:[2,3,0,1] row_mask:0xf bank_mask:0xf
	v_cndmask_b32_dpp v168, v172, v176, vcc quad_perm:[2,3,0,1] row_mask:0xf bank_mask:0xf
	v_cndmask_b32_dpp v161, v157, v165, vcc quad_perm:[2,3,0,1] row_mask:0xf bank_mask:0xf
	v_cndmask_b32_dpp v169, v173, v177, vcc quad_perm:[2,3,0,1] row_mask:0xf bank_mask:0xf
	s_mov_b32 vcc_lo, 0x33333333
	s_mov_b32 vcc_hi, 0x33333333
	s_nop 1
	v_cndmask_b32_dpp v154, v162, v154, vcc quad_perm:[2,3,0,1] row_mask:0xf bank_mask:0xf
	v_cndmask_b32_dpp v170, v174, v170, vcc quad_perm:[2,3,0,1] row_mask:0xf bank_mask:0xf
	v_cndmask_b32_dpp v155, v163, v155, vcc quad_perm:[2,3,0,1] row_mask:0xf bank_mask:0xf
	v_cndmask_b32_dpp v171, v175, v171, vcc quad_perm:[2,3,0,1] row_mask:0xf bank_mask:0xf
	v_cndmask_b32_dpp v156, v164, v156, vcc quad_perm:[2,3,0,1] row_mask:0xf bank_mask:0xf
	v_cndmask_b32_dpp v172, v176, v172, vcc quad_perm:[2,3,0,1] row_mask:0xf bank_mask:0xf
	v_cndmask_b32_dpp v157, v165, v157, vcc quad_perm:[2,3,0,1] row_mask:0xf bank_mask:0xf
	v_cndmask_b32_dpp v173, v177, v173, vcc quad_perm:[2,3,0,1] row_mask:0xf bank_mask:0xf
	global_store_dwordx4 v179, v[154:157], s[82:83]
	global_store_dwordx4 v180, v[170:173], s[82:83]
	global_store_dwordx4 v181, v[158:161], s[82:83]
	global_store_dwordx4 v190, v[166:169], s[82:83]

.Lhw_go_s1_0:
	s_add_u32 s100, s82, s69
	s_addc_u32 s101, s83, 0
	v_readlane_b32 s82, v239, 44
	v_readlane_b32 s83, v239, 45
	s_add_u32 s82, s82, s98
	s_addc_u32 s83, s83, 0
	global_load_dword v34, v178, s[100:101] nt
	s_add_u32 s100, s100, s89
	s_addc_u32 s101, s101, 0
	global_load_dword v35, v178, s[100:101] nt
	s_add_u32 s100, s100, s89
	s_addc_u32 s101, s101, 0
	global_load_dword v36, v178, s[100:101] nt
	s_add_u32 s100, s100, s89
	s_addc_u32 s101, s101, 0
	global_load_dword v37, v178, s[100:101] nt
	s_add_u32 s100, s100, s89
	s_addc_u32 s101, s101, 0
	global_load_dword v38, v178, s[100:101] nt
	s_add_u32 s100, s100, s89
	s_addc_u32 s101, s101, 0
	global_load_dword v39, v178, s[100:101] nt
	s_add_u32 s100, s100, s89
	s_addc_u32 s101, s101, 0
	global_load_dword v40, v178, s[100:101] nt
	s_add_u32 s100, s100, s89
	s_addc_u32 s101, s101, 0
	global_load_dword v41, v178, s[100:101] nt
	s_add_u32 s100, s100, s89
	s_addc_u32 s101, s101, 0
	global_load_dword v42, v178, s[100:101] nt
	s_add_u32 s100, s100, s89
	s_addc_u32 s101, s101, 0
	global_load_dword v43, v178, s[100:101] nt
	s_add_u32 s100, s100, s89
	s_addc_u32 s101, s101, 0
	global_load_dword v44, v178, s[100:101] nt
	s_add_u32 s100, s100, s89
	s_addc_u32 s101, s101, 0
	global_load_dword v45, v178, s[100:101] nt
	s_add_u32 s100, s100, s89
	s_addc_u32 s101, s101, 0
	global_load_dword v46, v178, s[100:101] nt
	s_add_u32 s100, s100, s89
	s_addc_u32 s101, s101, 0
	global_load_dword v47, v178, s[100:101] nt
	s_add_u32 s100, s100, s89
	s_addc_u32 s101, s101, 0
	global_load_dword v48, v178, s[100:101] nt
	s_add_u32 s100, s100, s89
	s_addc_u32 s101, s101, 0
	global_load_dword v49, v178, s[100:101] nt
	s_add_u32 s100, s100, s89
	s_addc_u32 s101, s101, 0
	global_load_dword v50, v178, s[100:101] nt
	s_add_u32 s100, s100, s89
	s_addc_u32 s101, s101, 0
	global_load_dword v51, v178, s[100:101] nt
	s_add_u32 s100, s100, s89
	s_addc_u32 s101, s101, 0
	global_load_dword v52, v178, s[100:101] nt
	s_add_u32 s100, s100, s89
	s_addc_u32 s101, s101, 0
	global_load_dword v53, v178, s[100:101] nt
	s_add_u32 s100, s100, s89
	s_addc_u32 s101, s101, 0
	global_load_dword v54, v178, s[100:101] nt
	s_add_u32 s100, s100, s89
	s_addc_u32 s101, s101, 0
	global_load_dword v55, v178, s[100:101] nt
	s_add_u32 s100, s100, s89
	s_addc_u32 s101, s101, 0
	global_load_dword v56, v178, s[100:101] nt
	s_add_u32 s100, s100, s89
	s_addc_u32 s101, s101, 0
	global_load_dword v57, v178, s[100:101] nt
	s_add_u32 s100, s100, s89
	s_addc_u32 s101, s101, 0
	global_load_dword v58, v178, s[100:101] nt
	s_add_u32 s100, s100, s89
	s_addc_u32 s101, s101, 0
	global_load_dword v59, v178, s[100:101] nt
	s_add_u32 s100, s100, s89
	s_addc_u32 s101, s101, 0
	global_load_dword v60, v178, s[100:101] nt
	s_add_u32 s100, s100, s89
	s_addc_u32 s101, s101, 0
	global_load_dword v61, v178, s[100:101] nt
	s_add_u32 s100, s100, s89
	s_addc_u32 s101, s101, 0
	global_load_dword v62, v178, s[100:101] nt
	s_add_u32 s100, s100, s89
	s_addc_u32 s101, s101, 0
	global_load_dword v63, v178, s[100:101] nt
	s_add_u32 s100, s100, s89
	s_addc_u32 s101, s101, 0
	global_load_dword v64, v178, s[100:101] nt
	s_add_u32 s100, s100, s89
	s_addc_u32 s101, s101, 0
	global_load_dword v65, v178, s[100:101] nt
	s_add_u32 s100, s100, s89
	s_addc_u32 s101, s101, 0
	global_load_dword v66, v178, s[100:101] nt
	s_add_u32 s100, s100, s89
	s_addc_u32 s101, s101, 0
	global_load_dword v67, v178, s[100:101] nt
	s_add_u32 s100, s100, s89
	s_addc_u32 s101, s101, 0
	global_load_dword v68, v178, s[100:101] nt
	s_add_u32 s100, s100, s89
	s_addc_u32 s101, s101, 0
	global_load_dword v69, v178, s[100:101] nt
	s_add_u32 s100, s100, s89
	s_addc_u32 s101, s101, 0
	global_load_dword v70, v178, s[100:101] nt
	s_add_u32 s100, s100, s89
	s_addc_u32 s101, s101, 0
	global_load_dword v71, v178, s[100:101] nt
	s_add_u32 s100, s100, s89
	s_addc_u32 s101, s101, 0
	global_load_dword v72, v178, s[100:101] nt
	s_add_u32 s100, s100, s89
	s_addc_u32 s101, s101, 0
	global_load_dword v73, v178, s[100:101] nt
	s_add_u32 s100, s100, s89
	s_addc_u32 s101, s101, 0
	global_load_dword v74, v178, s[100:101] nt
	s_add_u32 s100, s100, s89
	s_addc_u32 s101, s101, 0
	global_load_dword v75, v178, s[100:101] nt
	s_add_u32 s100, s100, s89
	s_addc_u32 s101, s101, 0
	global_load_dword v76, v178, s[100:101] nt
	s_add_u32 s100, s100, s89
	s_addc_u32 s101, s101, 0
	global_load_dword v77, v178, s[100:101] nt
	s_add_u32 s100, s100, s89
	s_addc_u32 s101, s101, 0
	global_load_dword v78, v178, s[100:101] nt
	s_add_u32 s100, s100, s89
	s_addc_u32 s101, s101, 0
	global_load_dword v79, v178, s[100:101] nt
	s_add_u32 s100, s100, s89
	s_addc_u32 s101, s101, 0
	global_load_dword v80, v178, s[100:101] nt
	s_add_u32 s100, s100, s89
	s_addc_u32 s101, s101, 0
	global_load_dword v81, v178, s[100:101] nt
	s_add_u32 s100, s100, s89
	s_addc_u32 s101, s101, 0
	global_load_dword v82, v178, s[100:101] nt
	s_add_u32 s100, s100, s89
	s_addc_u32 s101, s101, 0
	global_load_dword v83, v178, s[100:101] nt
	s_add_u32 s100, s100, s89
	s_addc_u32 s101, s101, 0
	global_load_dword v84, v178, s[100:101] nt
	s_add_u32 s100, s100, s89
	s_addc_u32 s101, s101, 0
	global_load_dword v85, v178, s[100:101] nt
	s_add_u32 s100, s100, s89
	s_addc_u32 s101, s101, 0
	global_load_dword v86, v178, s[100:101] nt
	s_add_u32 s100, s100, s89
	s_addc_u32 s101, s101, 0
	global_load_dword v87, v178, s[100:101] nt
	s_add_u32 s100, s100, s89
	s_addc_u32 s101, s101, 0
	global_load_dword v88, v178, s[100:101] nt
	s_add_u32 s100, s100, s89
	s_addc_u32 s101, s101, 0
	global_load_dword v89, v178, s[100:101] nt
	s_add_u32 s100, s100, s89
	s_addc_u32 s101, s101, 0
	global_load_dword v90, v178, s[100:101] nt
	s_add_u32 s100, s100, s89
	s_addc_u32 s101, s101, 0
	global_load_dword v91, v178, s[100:101] nt
	s_add_u32 s100, s100, s89
	s_addc_u32 s101, s101, 0
	global_load_dword v92, v178, s[100:101] nt
	s_add_u32 s100, s100, s89
	s_addc_u32 s101, s101, 0
	global_load_dword v93, v178, s[100:101] nt
	s_add_u32 s100, s100, s89
	s_addc_u32 s101, s101, 0
	global_load_dword v94, v178, s[100:101] nt
	s_add_u32 s100, s100, s89
	s_addc_u32 s101, s101, 0
	global_load_dword v95, v178, s[100:101] nt
	s_add_u32 s100, s100, s89
	s_addc_u32 s101, s101, 0
	global_load_dword v96, v178, s[100:101] nt
	s_add_u32 s100, s100, s89
	s_addc_u32 s101, s101, 0
	global_load_dword v97, v178, s[100:101] nt
	s_add_u32 s100, s100, s89
	s_addc_u32 s101, s101, 0
	s_waitcnt vmcnt(48)
	v_mul_f32_e32 v34, 0x42000000, v34
	v_mul_f32_e32 v35, 0x42000000, v35
	v_mul_f32_e32 v36, 0x42000000, v36
	v_mul_f32_e32 v37, 0x42000000, v37
	v_mul_f32_e32 v38, 0x42000000, v38
	v_mul_f32_e32 v39, 0x42000000, v39
	v_mul_f32_e32 v40, 0x42000000, v40
	v_mul_f32_e32 v41, 0x42000000, v41
	v_mul_f32_e32 v42, 0x42000000, v42
	v_mul_f32_e32 v43, 0x42000000, v43
	v_mul_f32_e32 v44, 0x42000000, v44
	v_mul_f32_e32 v45, 0x42000000, v45
	v_mul_f32_e32 v46, 0x42000000, v46
	v_mul_f32_e32 v47, 0x42000000, v47
	v_mul_f32_e32 v48, 0x42000000, v48
	v_mul_f32_e32 v49, 0x42000000, v49
	v_cvt_pk_fp8_f32 v154, v34, v35
	v_cvt_pk_fp8_f32 v155, v38, v39
	v_cvt_pk_fp8_f32 v156, v42, v43
	v_cvt_pk_fp8_f32 v157, v46, v47
	v_cvt_pk_fp8_f32 v154, v36, v37 op_sel:[0,0,1]
	v_cvt_pk_fp8_f32 v155, v40, v41 op_sel:[0,0,1]
	v_cvt_pk_fp8_f32 v156, v44, v45 op_sel:[0,0,1]
	v_cvt_pk_fp8_f32 v157, v48, v49 op_sel:[0,0,1]
	s_waitcnt vmcnt(32)
	v_mul_f32_e32 v50, 0x42000000, v50
	v_mul_f32_e32 v51, 0x42000000, v51
	v_mul_f32_e32 v52, 0x42000000, v52
	v_mul_f32_e32 v53, 0x42000000, v53
	v_mul_f32_e32 v54, 0x42000000, v54
	v_mul_f32_e32 v55, 0x42000000, v55
	v_mul_f32_e32 v56, 0x42000000, v56
	v_mul_f32_e32 v57, 0x42000000, v57
	v_mul_f32_e32 v58, 0x42000000, v58
	v_mul_f32_e32 v59, 0x42000000, v59
	v_mul_f32_e32 v60, 0x42000000, v60
	v_mul_f32_e32 v61, 0x42000000, v61
	v_mul_f32_e32 v62, 0x42000000, v62
	v_mul_f32_e32 v63, 0x42000000, v63
	v_mul_f32_e32 v64, 0x42000000, v64
	v_mul_f32_e32 v65, 0x42000000, v65
	v_cvt_pk_fp8_f32 v158, v50, v51
	v_cvt_pk_fp8_f32 v159, v54, v55
	v_cvt_pk_fp8_f32 v160, v58, v59
	v_cvt_pk_fp8_f32 v161, v62, v63
	v_cvt_pk_fp8_f32 v158, v52, v53 op_sel:[0,0,1]
	v_cvt_pk_fp8_f32 v159, v56, v57 op_sel:[0,0,1]
	v_cvt_pk_fp8_f32 v160, v60, v61 op_sel:[0,0,1]
	v_cvt_pk_fp8_f32 v161, v64, v65 op_sel:[0,0,1]
	s_waitcnt vmcnt(16)
	v_mul_f32_e32 v66, 0x42000000, v66
	v_mul_f32_e32 v67, 0x42000000, v67
	v_mul_f32_e32 v68, 0x42000000, v68
	v_mul_f32_e32 v69, 0x42000000, v69
	v_mul_f32_e32 v70, 0x42000000, v70
	v_mul_f32_e32 v71, 0x42000000, v71
	v_mul_f32_e32 v72, 0x42000000, v72
	v_mul_f32_e32 v73, 0x42000000, v73
	v_mul_f32_e32 v74, 0x42000000, v74
	v_mul_f32_e32 v75, 0x42000000, v75
	v_mul_f32_e32 v76, 0x42000000, v76
	v_mul_f32_e32 v77, 0x42000000, v77
	v_mul_f32_e32 v78, 0x42000000, v78
	v_mul_f32_e32 v79, 0x42000000, v79
	v_mul_f32_e32 v80, 0x42000000, v80
	v_mul_f32_e32 v81, 0x42000000, v81
	v_cvt_pk_fp8_f32 v162, v66, v67
	v_cvt_pk_fp8_f32 v163, v70, v71
	v_cvt_pk_fp8_f32 v164, v74, v75
	v_cvt_pk_fp8_f32 v165, v78, v79
	v_cvt_pk_fp8_f32 v162, v68, v69 op_sel:[0,0,1]
	v_cvt_pk_fp8_f32 v163, v72, v73 op_sel:[0,0,1]
	v_cvt_pk_fp8_f32 v164, v76, v77 op_sel:[0,0,1]
	v_cvt_pk_fp8_f32 v165, v80, v81 op_sel:[0,0,1]
	s_waitcnt vmcnt(0)
	v_mul_f32_e32 v82, 0x42000000, v82
	v_mul_f32_e32 v83, 0x42000000, v83
	v_mul_f32_e32 v84, 0x42000000, v84
	v_mul_f32_e32 v85, 0x42000000, v85
	v_mul_f32_e32 v86, 0x42000000, v86
	v_mul_f32_e32 v87, 0x42000000, v87
	v_mul_f32_e32 v88, 0x42000000, v88
	v_mul_f32_e32 v89, 0x42000000, v89
	v_mul_f32_e32 v90, 0x42000000, v90
	v_mul_f32_e32 v91, 0x42000000, v91
	v_mul_f32_e32 v92, 0x42000000, v92
	v_mul_f32_e32 v93, 0x42000000, v93
	v_mul_f32_e32 v94, 0x42000000, v94
	v_mul_f32_e32 v95, 0x42000000, v95
	v_mul_f32_e32 v96, 0x42000000, v96
	v_mul_f32_e32 v97, 0x42000000, v97
	v_cvt_pk_fp8_f32 v166, v82, v83
	v_cvt_pk_fp8_f32 v167, v86, v87
	v_cvt_pk_fp8_f32 v168, v90, v91
	v_cvt_pk_fp8_f32 v169, v94, v95
	v_cvt_pk_fp8_f32 v166, v84, v85 op_sel:[0,0,1]
	v_cvt_pk_fp8_f32 v167, v88, v89 op_sel:[0,0,1]
	v_cvt_pk_fp8_f32 v168, v92, v93 op_sel:[0,0,1]
	v_cvt_pk_fp8_f32 v169, v96, v97 op_sel:[0,0,1]
	s_mov_b32 vcc_lo, 0xaaaaaaaa
	s_mov_b32 vcc_hi, 0xaaaaaaaa
	s_nop 1
	v_cndmask_b32_dpp v170, v154, v158, vcc quad_perm:[1,0,3,2] row_mask:0xf bank_mask:0xf
	v_cndmask_b32_dpp v174, v162, v166, vcc quad_perm:[1,0,3,2] row_mask:0xf bank_mask:0xf
	v_cndmask_b32_dpp v171, v155, v159, vcc quad_perm:[1,0,3,2] row_mask:0xf bank_mask:0xf
	v_cndmask_b32_dpp v175, v163, v167, vcc quad_perm:[1,0,3,2] row_mask:0xf bank_mask:0xf
	v_cndmask_b32_dpp v172, v156, v160, vcc quad_perm:[1,0,3,2] row_mask:0xf bank_mask:0xf
	v_cndmask_b32_dpp v176, v164, v168, vcc quad_perm:[1,0,3,2] row_mask:0xf bank_mask:0xf
	v_cndmask_b32_dpp v173, v157, v161, vcc quad_perm:[1,0,3,2] row_mask:0xf bank_mask:0xf
	v_cndmask_b32_dpp v177, v165, v169, vcc quad_perm:[1,0,3,2] row_mask:0xf bank_mask:0xf
	s_mov_b32 vcc_lo, 0x55555555
	s_mov_b32 vcc_hi, 0x55555555
	s_nop 1
	v_cndmask_b32_dpp v154, v158, v154, vcc quad_perm:[1,0,3,2] row_mask:0xf bank_mask:0xf
	v_cndmask_b32_dpp v162, v166, v162, vcc quad_perm:[1,0,3,2] row_mask:0xf bank_mask:0xf
	v_cndmask_b32_dpp v155, v159, v155, vcc quad_perm:[1,0,3,2] row_mask:0xf bank_mask:0xf
	v_cndmask_b32_dpp v163, v167, v163, vcc quad_perm:[1,0,3,2] row_mask:0xf bank_mask:0xf
	v_cndmask_b32_dpp v156, v160, v156, vcc quad_perm:[1,0,3,2] row_mask:0xf bank_mask:0xf
	v_cndmask_b32_dpp v164, v168, v164, vcc quad_perm:[1,0,3,2] row_mask:0xf bank_mask:0xf
	v_cndmask_b32_dpp v157, v161, v157, vcc quad_perm:[1,0,3,2] row_mask:0xf bank_mask:0xf
	v_cndmask_b32_dpp v165, v169, v165, vcc quad_perm:[1,0,3,2] row_mask:0xf bank_mask:0xf
	s_mov_b32 vcc_lo, 0xcccccccc
	s_mov_b32 vcc_hi, 0xcccccccc
	s_nop 1
	v_cndmask_b32_dpp v158, v154, v162, vcc quad_perm:[2,3,0,1] row_mask:0xf bank_mask:0xf
	v_cndmask_b32_dpp v166, v170, v174, vcc quad_perm:[2,3,0,1] row_mask:0xf bank_mask:0xf
	v_cndmask_b32_dpp v159, v155, v163, vcc quad_perm:[2,3,0,1] row_mask:0xf bank_mask:0xf
	v_cndmask_b32_dpp v167, v171, v175, vcc quad_perm:[2,3,0,1] row_mask:0xf bank_mask:0xf
	v_cndmask_b32_dpp v160, v156, v164, vcc quad_perm:[2,3,0,1] row_mask:0xf bank_mask:0xf
	v_cndmask_b32_dpp v168, v172, v176, vcc quad_perm:[2,3,0,1] row_mask:0xf bank_mask:0xf
	v_cndmask_b32_dpp v161, v157, v165, vcc quad_perm:[2,3,0,1] row_mask:0xf bank_mask:0xf
	v_cndmask_b32_dpp v169, v173, v177, vcc quad_perm:[2,3,0,1] row_mask:0xf bank_mask:0xf
	s_mov_b32 vcc_lo, 0x33333333
	s_mov_b32 vcc_hi, 0x33333333
	s_nop 1
	v_cndmask_b32_dpp v154, v162, v154, vcc quad_perm:[2,3,0,1] row_mask:0xf bank_mask:0xf
	v_cndmask_b32_dpp v170, v174, v170, vcc quad_perm:[2,3,0,1] row_mask:0xf bank_mask:0xf
	v_cndmask_b32_dpp v155, v163, v155, vcc quad_perm:[2,3,0,1] row_mask:0xf bank_mask:0xf
	v_cndmask_b32_dpp v171, v175, v171, vcc quad_perm:[2,3,0,1] row_mask:0xf bank_mask:0xf
	v_cndmask_b32_dpp v156, v164, v156, vcc quad_perm:[2,3,0,1] row_mask:0xf bank_mask:0xf
	v_cndmask_b32_dpp v172, v176, v172, vcc quad_perm:[2,3,0,1] row_mask:0xf bank_mask:0xf
	v_cndmask_b32_dpp v157, v165, v157, vcc quad_perm:[2,3,0,1] row_mask:0xf bank_mask:0xf
	v_cndmask_b32_dpp v173, v177, v173, vcc quad_perm:[2,3,0,1] row_mask:0xf bank_mask:0xf
	global_store_dwordx4 v179, v[154:157], s[82:83]
	global_store_dwordx4 v180, v[170:173], s[82:83]
	global_store_dwordx4 v181, v[158:161], s[82:83]
	global_store_dwordx4 v190, v[166:169], s[82:83]
	v_readlane_b32 s2, v239, 0
	s_lshr_b32 s2, s2, 6
	s_add_i32 s2, s2, 6
	s_cmp_gt_u32 s2, 13
	s_cbranch_scc1 .Lhw_seam1_done
	s_add_i32 s2, s2, 14
	s_mul_i32 s2, s2, s74
	v_readlane_b32 s9, v239, 23
	s_lshr_b32 s9, s9, 3
	s_add_i32 s2, s2, s9
	s_cmp_gt_u32 s2, 24575
	s_cbranch_scc1 .Lhw_seam1_done
	v_mbcnt_lo_u32_b32 v178, -1, 0
	v_mbcnt_hi_u32_b32 v178, -1, v178
	v_and_b32_e32 v179, 60, v178
	v_lshlrev_b32_e32 v179, 10, v179
	v_and_b32_e32 v180, 3, v178
	v_lshl_or_b32 v179, v180, 4, v179
	v_add_u32_e32 v180, 0x400, v179
	v_add_u32_e32 v181, 0x800, v179
	v_add_u32_e32 v190, 0xc00, v179
	v_lshlrev_b32_e32 v178, 2, v178
	s_cmp_lt_u32 s2, 16384
	s_cbranch_scc0 .Lhw_dn_s1_1
	s_lshr_b32 s9, s2, 9
	s_bfe_u32 s32, s2, 0x40005
	s_and_b32 s53, s2, 31
	s_lshl_b32 s69, s9, 23
	s_lshl_b32 s100, s32, 19
	s_add_i32 s69, s69, s100
	s_lshl_b32 s100, s53, 8
	s_add_i32 s69, s69, s100
	s_lshl_b32 s98, s9, 11
	s_bfe_u32 s100, s53, 0x30001
	s_lshl_b32 s100, s100, 8
	s_add_i32 s98, s98, s100
	s_lshr_b32 s100, s53, 4
	s_lshl_b32 s100, s100, 7
	s_add_i32 s98, s98, s100
	s_and_b32 s100, s53, 1
	s_lshl_b32 s100, s100, 6
	s_add_i32 s98, s98, s100
	s_lshl_b32 s98, s98, 10
	s_lshl_b32 s100, s32, 6
	s_add_i32 s98, s98, s100
	s_add_i32 s98, s98, 0x2000000
	v_readlane_b32 s82, v239, 11
	v_readlane_b32 s83, v239, 12
	s_movk_i32 s89, 8192
	s_branch .Lhw_go_s1_1

.Lhw_go_s2_0:
	s_add_u32 s100, s82, s69
	s_addc_u32 s101, s83, 0
	v_readlane_b32 s82, v239, 44
	v_readlane_b32 s83, v239, 45
	s_add_u32 s82, s82, s98
	s_addc_u32 s83, s83, 0
	global_load_dword v34, v178, s[100:101] nt
	s_add_u32 s100, s100, s89
	s_addc_u32 s101, s101, 0
	global_load_dword v35, v178, s[100:101] nt
	s_add_u32 s100, s100, s89
	s_addc_u32 s101, s101, 0
	global_load_dword v36, v178, s[100:101] nt
	s_add_u32 s100, s100, s89
	s_addc_u32 s101, s101, 0
	global_load_dword v37, v178, s[100:101] nt
	s_add_u32 s100, s100, s89
	s_addc_u32 s101, s101, 0
	global_load_dword v38, v178, s[100:101] nt
	s_add_u32 s100, s100, s89
	s_addc_u32 s101, s101, 0
	global_load_dword v39, v178, s[100:101] nt
	s_add_u32 s100, s100, s89
	s_addc_u32 s101, s101, 0
	global_load_dword v40, v178, s[100:101] nt
	s_add_u32 s100, s100, s89
	s_addc_u32 s101, s101, 0
	global_load_dword v41, v178, s[100:101] nt
	s_add_u32 s100, s100, s89
	s_addc_u32 s101, s101, 0
	global_load_dword v42, v178, s[100:101] nt
	s_add_u32 s100, s100, s89
	s_addc_u32 s101, s101, 0
	global_load_dword v43, v178, s[100:101] nt
	s_add_u32 s100, s100, s89
	s_addc_u32 s101, s101, 0
	global_load_dword v44, v178, s[100:101] nt
	s_add_u32 s100, s100, s89
	s_addc_u32 s101, s101, 0
	global_load_dword v45, v178, s[100:101] nt
	s_add_u32 s100, s100, s89
	s_addc_u32 s101, s101, 0
	global_load_dword v46, v178, s[100:101] nt
	s_add_u32 s100, s100, s89
	s_addc_u32 s101, s101, 0
	global_load_dword v47, v178, s[100:101] nt
	s_add_u32 s100, s100, s89
	s_addc_u32 s101, s101, 0
	global_load_dword v48, v178, s[100:101] nt
	s_add_u32 s100, s100, s89
	s_addc_u32 s101, s101, 0
	global_load_dword v49, v178, s[100:101] nt
	s_add_u32 s100, s100, s89
	s_addc_u32 s101, s101, 0
	global_load_dword v50, v178, s[100:101] nt
	s_add_u32 s100, s100, s89
	s_addc_u32 s101, s101, 0
	global_load_dword v51, v178, s[100:101] nt
	s_add_u32 s100, s100, s89
	s_addc_u32 s101, s101, 0
	global_load_dword v52, v178, s[100:101] nt
	s_add_u32 s100, s100, s89
	s_addc_u32 s101, s101, 0
	global_load_dword v53, v178, s[100:101] nt
	s_add_u32 s100, s100, s89
	s_addc_u32 s101, s101, 0
	global_load_dword v54, v178, s[100:101] nt
	s_add_u32 s100, s100, s89
	s_addc_u32 s101, s101, 0
	global_load_dword v55, v178, s[100:101] nt
	s_add_u32 s100, s100, s89
	s_addc_u32 s101, s101, 0
	global_load_dword v56, v178, s[100:101] nt
	s_add_u32 s100, s100, s89
	s_addc_u32 s101, s101, 0
	global_load_dword v57, v178, s[100:101] nt
	s_add_u32 s100, s100, s89
	s_addc_u32 s101, s101, 0
	global_load_dword v58, v178, s[100:101] nt
	s_add_u32 s100, s100, s89
	s_addc_u32 s101, s101, 0
	global_load_dword v59, v178, s[100:101] nt
	s_add_u32 s100, s100, s89
	s_addc_u32 s101, s101, 0
	global_load_dword v60, v178, s[100:101] nt
	s_add_u32 s100, s100, s89
	s_addc_u32 s101, s101, 0
	global_load_dword v61, v178, s[100:101] nt
	s_add_u32 s100, s100, s89
	s_addc_u32 s101, s101, 0
	global_load_dword v62, v178, s[100:101] nt
	s_add_u32 s100, s100, s89
	s_addc_u32 s101, s101, 0
	global_load_dword v63, v178, s[100:101] nt
	s_add_u32 s100, s100, s89
	s_addc_u32 s101, s101, 0
	global_load_dword v64, v178, s[100:101] nt
	s_add_u32 s100, s100, s89
	s_addc_u32 s101, s101, 0
	global_load_dword v65, v178, s[100:101] nt
	s_add_u32 s100, s100, s89
	s_addc_u32 s101, s101, 0
	global_load_dword v66, v178, s[100:101] nt
	s_add_u32 s100, s100, s89
	s_addc_u32 s101, s101, 0
	global_load_dword v67, v178, s[100:101] nt
	s_add_u32 s100, s100, s89
	s_addc_u32 s101, s101, 0
	global_load_dword v68, v178, s[100:101] nt
	s_add_u32 s100, s100, s89
	s_addc_u32 s101, s101, 0
	global_load_dword v69, v178, s[100:101] nt
	s_add_u32 s100, s100, s89
	s_addc_u32 s101, s101, 0
	global_load_dword v70, v178, s[100:101] nt
	s_add_u32 s100, s100, s89
	s_addc_u32 s101, s101, 0
	global_load_dword v71, v178, s[100:101] nt
	s_add_u32 s100, s100, s89
	s_addc_u32 s101, s101, 0
	global_load_dword v72, v178, s[100:101] nt
	s_add_u32 s100, s100, s89
	s_addc_u32 s101, s101, 0
	global_load_dword v73, v178, s[100:101] nt
	s_add_u32 s100, s100, s89
	s_addc_u32 s101, s101, 0
	global_load_dword v74, v178, s[100:101] nt
	s_add_u32 s100, s100, s89
	s_addc_u32 s101, s101, 0
	global_load_dword v75, v178, s[100:101] nt
	s_add_u32 s100, s100, s89
	s_addc_u32 s101, s101, 0
	global_load_dword v76, v178, s[100:101] nt
	s_add_u32 s100, s100, s89
	s_addc_u32 s101, s101, 0
	global_load_dword v77, v178, s[100:101] nt
	s_add_u32 s100, s100, s89
	s_addc_u32 s101, s101, 0
	global_load_dword v78, v178, s[100:101] nt
	s_add_u32 s100, s100, s89
	s_addc_u32 s101, s101, 0
	global_load_dword v79, v178, s[100:101] nt
	s_add_u32 s100, s100, s89
	s_addc_u32 s101, s101, 0
	global_load_dword v80, v178, s[100:101] nt
	s_add_u32 s100, s100, s89
	s_addc_u32 s101, s101, 0
	global_load_dword v81, v178, s[100:101] nt
	s_add_u32 s100, s100, s89
	s_addc_u32 s101, s101, 0
	global_load_dword v82, v178, s[100:101] nt
	s_add_u32 s100, s100, s89
	s_addc_u32 s101, s101, 0
	global_load_dword v83, v178, s[100:101] nt
	s_add_u32 s100, s100, s89
	s_addc_u32 s101, s101, 0
	global_load_dword v84, v178, s[100:101] nt
	s_add_u32 s100, s100, s89
	s_addc_u32 s101, s101, 0
	global_load_dword v85, v178, s[100:101] nt
	s_add_u32 s100, s100, s89
	s_addc_u32 s101, s101, 0
	global_load_dword v86, v178, s[100:101] nt
	s_add_u32 s100, s100, s89
	s_addc_u32 s101, s101, 0
	global_load_dword v87, v178, s[100:101] nt
	s_add_u32 s100, s100, s89
	s_addc_u32 s101, s101, 0
	global_load_dword v88, v178, s[100:101] nt
	s_add_u32 s100, s100, s89
	s_addc_u32 s101, s101, 0
	global_load_dword v89, v178, s[100:101] nt
	s_add_u32 s100, s100, s89
	s_addc_u32 s101, s101, 0
	global_load_dword v90, v178, s[100:101] nt
	s_add_u32 s100, s100, s89
	s_addc_u32 s101, s101, 0
	global_load_dword v91, v178, s[100:101] nt
	s_add_u32 s100, s100, s89
	s_addc_u32 s101, s101, 0
	global_load_dword v92, v178, s[100:101] nt
	s_add_u32 s100, s100, s89
	s_addc_u32 s101, s101, 0
	global_load_dword v93, v178, s[100:101] nt
	s_add_u32 s100, s100, s89
	s_addc_u32 s101, s101, 0
	global_load_dword v94, v178, s[100:101] nt
	s_add_u32 s100, s100, s89
	s_addc_u32 s101, s101, 0
	global_load_dword v95, v178, s[100:101] nt
	s_add_u32 s100, s100, s89
	s_addc_u32 s101, s101, 0
	global_load_dword v96, v178, s[100:101] nt
	s_add_u32 s100, s100, s89
	s_addc_u32 s101, s101, 0
	global_load_dword v97, v178, s[100:101] nt
	s_add_u32 s100, s100, s89
	s_addc_u32 s101, s101, 0
	s_waitcnt vmcnt(48)
	v_mul_f32_e32 v34, 0x42000000, v34
	v_mul_f32_e32 v35, 0x42000000, v35
	v_mul_f32_e32 v36, 0x42000000, v36
	v_mul_f32_e32 v37, 0x42000000, v37
	v_mul_f32_e32 v38, 0x42000000, v38
	v_mul_f32_e32 v39, 0x42000000, v39
	v_mul_f32_e32 v40, 0x42000000, v40
	v_mul_f32_e32 v41, 0x42000000, v41
	v_mul_f32_e32 v42, 0x42000000, v42
	v_mul_f32_e32 v43, 0x42000000, v43
	v_mul_f32_e32 v44, 0x42000000, v44
	v_mul_f32_e32 v45, 0x42000000, v45
	v_mul_f32_e32 v46, 0x42000000, v46
	v_mul_f32_e32 v47, 0x42000000, v47
	v_mul_f32_e32 v48, 0x42000000, v48
	v_mul_f32_e32 v49, 0x42000000, v49
	v_cvt_pk_fp8_f32 v154, v34, v35
	v_cvt_pk_fp8_f32 v155, v38, v39
	v_cvt_pk_fp8_f32 v156, v42, v43
	v_cvt_pk_fp8_f32 v157, v46, v47
	v_cvt_pk_fp8_f32 v154, v36, v37 op_sel:[0,0,1]
	v_cvt_pk_fp8_f32 v155, v40, v41 op_sel:[0,0,1]
	v_cvt_pk_fp8_f32 v156, v44, v45 op_sel:[0,0,1]
	v_cvt_pk_fp8_f32 v157, v48, v49 op_sel:[0,0,1]
	s_waitcnt vmcnt(32)
	v_mul_f32_e32 v50, 0x42000000, v50
	v_mul_f32_e32 v51, 0x42000000, v51
	v_mul_f32_e32 v52, 0x42000000, v52
	v_mul_f32_e32 v53, 0x42000000, v53
	v_mul_f32_e32 v54, 0x42000000, v54
	v_mul_f32_e32 v55, 0x42000000, v55
	v_mul_f32_e32 v56, 0x42000000, v56
	v_mul_f32_e32 v57, 0x42000000, v57
	v_mul_f32_e32 v58, 0x42000000, v58
	v_mul_f32_e32 v59, 0x42000000, v59
	v_mul_f32_e32 v60, 0x42000000, v60
	v_mul_f32_e32 v61, 0x42000000, v61
	v_mul_f32_e32 v62, 0x42000000, v62
	v_mul_f32_e32 v63, 0x42000000, v63
	v_mul_f32_e32 v64, 0x42000000, v64
	v_mul_f32_e32 v65, 0x42000000, v65
	v_cvt_pk_fp8_f32 v158, v50, v51
	v_cvt_pk_fp8_f32 v159, v54, v55
	v_cvt_pk_fp8_f32 v160, v58, v59
	v_cvt_pk_fp8_f32 v161, v62, v63
	v_cvt_pk_fp8_f32 v158, v52, v53 op_sel:[0,0,1]
	v_cvt_pk_fp8_f32 v159, v56, v57 op_sel:[0,0,1]
	v_cvt_pk_fp8_f32 v160, v60, v61 op_sel:[0,0,1]
	v_cvt_pk_fp8_f32 v161, v64, v65 op_sel:[0,0,1]
	s_waitcnt vmcnt(16)
	v_mul_f32_e32 v66, 0x42000000, v66
	v_mul_f32_e32 v67, 0x42000000, v67
	v_mul_f32_e32 v68, 0x42000000, v68
	v_mul_f32_e32 v69, 0x42000000, v69
	v_mul_f32_e32 v70, 0x42000000, v70
	v_mul_f32_e32 v71, 0x42000000, v71
	v_mul_f32_e32 v72, 0x42000000, v72
	v_mul_f32_e32 v73, 0x42000000, v73
	v_mul_f32_e32 v74, 0x42000000, v74
	v_mul_f32_e32 v75, 0x42000000, v75
	v_mul_f32_e32 v76, 0x42000000, v76
	v_mul_f32_e32 v77, 0x42000000, v77
	v_mul_f32_e32 v78, 0x42000000, v78
	v_mul_f32_e32 v79, 0x42000000, v79
	v_mul_f32_e32 v80, 0x42000000, v80
	v_mul_f32_e32 v81, 0x42000000, v81
	v_cvt_pk_fp8_f32 v162, v66, v67
	v_cvt_pk_fp8_f32 v163, v70, v71
	v_cvt_pk_fp8_f32 v164, v74, v75
	v_cvt_pk_fp8_f32 v165, v78, v79
	v_cvt_pk_fp8_f32 v162, v68, v69 op_sel:[0,0,1]
	v_cvt_pk_fp8_f32 v163, v72, v73 op_sel:[0,0,1]
	v_cvt_pk_fp8_f32 v164, v76, v77 op_sel:[0,0,1]
	v_cvt_pk_fp8_f32 v165, v80, v81 op_sel:[0,0,1]
	s_waitcnt vmcnt(0)
	v_mul_f32_e32 v82, 0x42000000, v82
	v_mul_f32_e32 v83, 0x42000000, v83
	v_mul_f32_e32 v84, 0x42000000, v84
	v_mul_f32_e32 v85, 0x42000000, v85
	v_mul_f32_e32 v86, 0x42000000, v86
	v_mul_f32_e32 v87, 0x42000000, v87
	v_mul_f32_e32 v88, 0x42000000, v88
	v_mul_f32_e32 v89, 0x42000000, v89
	v_mul_f32_e32 v90, 0x42000000, v90
	v_mul_f32_e32 v91, 0x42000000, v91
	v_mul_f32_e32 v92, 0x42000000, v92
	v_mul_f32_e32 v93, 0x42000000, v93
	v_mul_f32_e32 v94, 0x42000000, v94
	v_mul_f32_e32 v95, 0x42000000, v95
	v_mul_f32_e32 v96, 0x42000000, v96
	v_mul_f32_e32 v97, 0x42000000, v97
	v_cvt_pk_fp8_f32 v166, v82, v83
	v_cvt_pk_fp8_f32 v167, v86, v87
	v_cvt_pk_fp8_f32 v168, v90, v91
	v_cvt_pk_fp8_f32 v169, v94, v95
	v_cvt_pk_fp8_f32 v166, v84, v85 op_sel:[0,0,1]
	v_cvt_pk_fp8_f32 v167, v88, v89 op_sel:[0,0,1]
	v_cvt_pk_fp8_f32 v168, v92, v93 op_sel:[0,0,1]
	v_cvt_pk_fp8_f32 v169, v96, v97 op_sel:[0,0,1]
	s_mov_b32 vcc_lo, 0xaaaaaaaa
	s_mov_b32 vcc_hi, 0xaaaaaaaa
	s_nop 1
	v_cndmask_b32_dpp v170, v154, v158, vcc quad_perm:[1,0,3,2] row_mask:0xf bank_mask:0xf
	v_cndmask_b32_dpp v174, v162, v166, vcc quad_perm:[1,0,3,2] row_mask:0xf bank_mask:0xf
	v_cndmask_b32_dpp v171, v155, v159, vcc quad_perm:[1,0,3,2] row_mask:0xf bank_mask:0xf
	v_cndmask_b32_dpp v175, v163, v167, vcc quad_perm:[1,0,3,2] row_mask:0xf bank_mask:0xf
	v_cndmask_b32_dpp v172, v156, v160, vcc quad_perm:[1,0,3,2] row_mask:0xf bank_mask:0xf
	v_cndmask_b32_dpp v176, v164, v168, vcc quad_perm:[1,0,3,2] row_mask:0xf bank_mask:0xf
	v_cndmask_b32_dpp v173, v157, v161, vcc quad_perm:[1,0,3,2] row_mask:0xf bank_mask:0xf
	v_cndmask_b32_dpp v177, v165, v169, vcc quad_perm:[1,0,3,2] row_mask:0xf bank_mask:0xf
	s_mov_b32 vcc_lo, 0x55555555
	s_mov_b32 vcc_hi, 0x55555555
	s_nop 1
	v_cndmask_b32_dpp v154, v158, v154, vcc quad_perm:[1,0,3,2] row_mask:0xf bank_mask:0xf
	v_cndmask_b32_dpp v162, v166, v162, vcc quad_perm:[1,0,3,2] row_mask:0xf bank_mask:0xf
	v_cndmask_b32_dpp v155, v159, v155, vcc quad_perm:[1,0,3,2] row_mask:0xf bank_mask:0xf
	v_cndmask_b32_dpp v163, v167, v163, vcc quad_perm:[1,0,3,2] row_mask:0xf bank_mask:0xf
	v_cndmask_b32_dpp v156, v160, v156, vcc quad_perm:[1,0,3,2] row_mask:0xf bank_mask:0xf
	v_cndmask_b32_dpp v164, v168, v164, vcc quad_perm:[1,0,3,2] row_mask:0xf bank_mask:0xf
	v_cndmask_b32_dpp v157, v161, v157, vcc quad_perm:[1,0,3,2] row_mask:0xf bank_mask:0xf
	v_cndmask_b32_dpp v165, v169, v165, vcc quad_perm:[1,0,3,2] row_mask:0xf bank_mask:0xf
	s_mov_b32 vcc_lo, 0xcccccccc
	s_mov_b32 vcc_hi, 0xcccccccc
	s_nop 1
	v_cndmask_b32_dpp v158, v154, v162, vcc quad_perm:[2,3,0,1] row_mask:0xf bank_mask:0xf
	v_cndmask_b32_dpp v166, v170, v174, vcc quad_perm:[2,3,0,1] row_mask:0xf bank_mask:0xf
	v_cndmask_b32_dpp v159, v155, v163, vcc quad_perm:[2,3,0,1] row_mask:0xf bank_mask:0xf
	v_cndmask_b32_dpp v167, v171, v175, vcc quad_perm:[2,3,0,1] row_mask:0xf bank_mask:0xf
	v_cndmask_b32_dpp v160, v156, v164, vcc quad_perm:[2,3,0,1] row_mask:0xf bank_mask:0xf
	v_cndmask_b32_dpp v168, v172, v176, vcc quad_perm:[2,3,0,1] row_mask:0xf bank_mask:0xf
	v_cndmask_b32_dpp v161, v157, v165, vcc quad_perm:[2,3,0,1] row_mask:0xf bank_mask:0xf
	v_cndmask_b32_dpp v169, v173, v177, vcc quad_perm:[2,3,0,1] row_mask:0xf bank_mask:0xf
	s_mov_b32 vcc_lo, 0x33333333
	s_mov_b32 vcc_hi, 0x33333333
	s_nop 1
	v_cndmask_b32_dpp v154, v162, v154, vcc quad_perm:[2,3,0,1] row_mask:0xf bank_mask:0xf
	v_cndmask_b32_dpp v170, v174, v170, vcc quad_perm:[2,3,0,1] row_mask:0xf bank_mask:0xf
	v_cndmask_b32_dpp v155, v163, v155, vcc quad_perm:[2,3,0,1] row_mask:0xf bank_mask:0xf
	v_cndmask_b32_dpp v171, v175, v171, vcc quad_perm:[2,3,0,1] row_mask:0xf bank_mask:0xf
	v_cndmask_b32_dpp v156, v164, v156, vcc quad_perm:[2,3,0,1] row_mask:0xf bank_mask:0xf
	v_cndmask_b32_dpp v172, v176, v172, vcc quad_perm:[2,3,0,1] row_mask:0xf bank_mask:0xf
	v_cndmask_b32_dpp v157, v165, v157, vcc quad_perm:[2,3,0,1] row_mask:0xf bank_mask:0xf
	v_cndmask_b32_dpp v173, v177, v173, vcc quad_perm:[2,3,0,1] row_mask:0xf bank_mask:0xf
	global_store_dwordx4 v179, v[154:157], s[82:83]
	global_store_dwordx4 v180, v[170:173], s[82:83]
	global_store_dwordx4 v181, v[158:161], s[82:83]
	global_store_dwordx4 v190, v[166:169], s[82:83]
	v_readlane_b32 s2, v239, 0
	s_lshr_b32 s2, s2, 6
	s_add_i32 s2, s2, 6
	s_cmp_gt_u32 s2, 13
	s_cbranch_scc1 .Lhw_seam2_done
	s_add_i32 s2, s2, 28
	s_mul_i32 s2, s2, s74
	v_readlane_b32 s9, v239, 23
	s_lshr_b32 s9, s9, 3
	s_add_i32 s2, s2, s9
	s_cmp_gt_u32 s2, 24575
	s_cbranch_scc1 .Lhw_seam2_done
	v_mbcnt_lo_u32_b32 v178, -1, 0
	v_mbcnt_hi_u32_b32 v178, -1, v178
	v_and_b32_e32 v179, 60, v178
	v_lshlrev_b32_e32 v179, 10, v179
	v_and_b32_e32 v180, 3, v178
	v_lshl_or_b32 v179, v180, 4, v179
	v_add_u32_e32 v180, 0x400, v179
	v_add_u32_e32 v181, 0x800, v179
	v_add_u32_e32 v190, 0xc00, v179
	v_lshlrev_b32_e32 v178, 2, v178
	s_cmp_lt_u32 s2, 16384
	s_cbranch_scc0 .Lhw_dn_s2_1
	s_lshr_b32 s9, s2, 9
	s_bfe_u32 s32, s2, 0x40005
	s_and_b32 s53, s2, 31
	s_lshl_b32 s69, s9, 23
	s_lshl_b32 s100, s32, 19
	s_add_i32 s69, s69, s100
	s_lshl_b32 s100, s53, 8
	s_add_i32 s69, s69, s100
	s_lshl_b32 s98, s9, 11
	s_bfe_u32 s100, s53, 0x30001
	s_lshl_b32 s100, s100, 8
	s_add_i32 s98, s98, s100
	s_lshr_b32 s100, s53, 4
	s_lshl_b32 s100, s100, 7
	s_add_i32 s98, s98, s100
	s_and_b32 s100, s53, 1
	s_lshl_b32 s100, s100, 6
	s_add_i32 s98, s98, s100
	s_lshl_b32 s98, s98, 10
	s_lshl_b32 s100, s32, 6
	s_add_i32 s98, s98, s100
	s_add_i32 s98, s98, 0x2000000
	v_readlane_b32 s82, v239, 11
	v_readlane_b32 s83, v239, 12
	s_movk_i32 s89, 8192
	s_branch .Lhw_go_s2_1

.Lhw_go_s3_0:
	s_add_u32 s100, s82, s69
	s_addc_u32 s101, s83, 0
	v_readlane_b32 s82, v239, 44
	v_readlane_b32 s83, v239, 45
	s_add_u32 s82, s82, s98
	s_addc_u32 s83, s83, 0
	global_load_dword v34, v178, s[100:101] nt
	s_add_u32 s100, s100, s89
	s_addc_u32 s101, s101, 0
	global_load_dword v35, v178, s[100:101] nt
	s_add_u32 s100, s100, s89
	s_addc_u32 s101, s101, 0
	global_load_dword v36, v178, s[100:101] nt
	s_add_u32 s100, s100, s89
	s_addc_u32 s101, s101, 0
	global_load_dword v37, v178, s[100:101] nt
	s_add_u32 s100, s100, s89
	s_addc_u32 s101, s101, 0
	global_load_dword v38, v178, s[100:101] nt
	s_add_u32 s100, s100, s89
	s_addc_u32 s101, s101, 0
	global_load_dword v39, v178, s[100:101] nt
	s_add_u32 s100, s100, s89
	s_addc_u32 s101, s101, 0
	global_load_dword v40, v178, s[100:101] nt
	s_add_u32 s100, s100, s89
	s_addc_u32 s101, s101, 0
	global_load_dword v41, v178, s[100:101] nt
	s_add_u32 s100, s100, s89
	s_addc_u32 s101, s101, 0
	global_load_dword v42, v178, s[100:101] nt
	s_add_u32 s100, s100, s89
	s_addc_u32 s101, s101, 0
	global_load_dword v43, v178, s[100:101] nt
	s_add_u32 s100, s100, s89
	s_addc_u32 s101, s101, 0
	global_load_dword v44, v178, s[100:101] nt
	s_add_u32 s100, s100, s89
	s_addc_u32 s101, s101, 0
	global_load_dword v45, v178, s[100:101] nt
	s_add_u32 s100, s100, s89
	s_addc_u32 s101, s101, 0
	global_load_dword v46, v178, s[100:101] nt
	s_add_u32 s100, s100, s89
	s_addc_u32 s101, s101, 0
	global_load_dword v47, v178, s[100:101] nt
	s_add_u32 s100, s100, s89
	s_addc_u32 s101, s101, 0
	global_load_dword v48, v178, s[100:101] nt
	s_add_u32 s100, s100, s89
	s_addc_u32 s101, s101, 0
	global_load_dword v49, v178, s[100:101] nt
	s_add_u32 s100, s100, s89
	s_addc_u32 s101, s101, 0
	global_load_dword v50, v178, s[100:101] nt
	s_add_u32 s100, s100, s89
	s_addc_u32 s101, s101, 0
	global_load_dword v51, v178, s[100:101] nt
	s_add_u32 s100, s100, s89
	s_addc_u32 s101, s101, 0
	global_load_dword v52, v178, s[100:101] nt
	s_add_u32 s100, s100, s89
	s_addc_u32 s101, s101, 0
	global_load_dword v53, v178, s[100:101] nt
	s_add_u32 s100, s100, s89
	s_addc_u32 s101, s101, 0
	global_load_dword v54, v178, s[100:101] nt
	s_add_u32 s100, s100, s89
	s_addc_u32 s101, s101, 0
	global_load_dword v55, v178, s[100:101] nt
	s_add_u32 s100, s100, s89
	s_addc_u32 s101, s101, 0
	global_load_dword v56, v178, s[100:101] nt
	s_add_u32 s100, s100, s89
	s_addc_u32 s101, s101, 0
	global_load_dword v57, v178, s[100:101] nt
	s_add_u32 s100, s100, s89
	s_addc_u32 s101, s101, 0
	global_load_dword v58, v178, s[100:101] nt
	s_add_u32 s100, s100, s89
	s_addc_u32 s101, s101, 0
	global_load_dword v59, v178, s[100:101] nt
	s_add_u32 s100, s100, s89
	s_addc_u32 s101, s101, 0
	global_load_dword v60, v178, s[100:101] nt
	s_add_u32 s100, s100, s89
	s_addc_u32 s101, s101, 0
	global_load_dword v61, v178, s[100:101] nt
	s_add_u32 s100, s100, s89
	s_addc_u32 s101, s101, 0
	global_load_dword v62, v178, s[100:101] nt
	s_add_u32 s100, s100, s89
	s_addc_u32 s101, s101, 0
	global_load_dword v63, v178, s[100:101] nt
	s_add_u32 s100, s100, s89
	s_addc_u32 s101, s101, 0
	global_load_dword v64, v178, s[100:101] nt
	s_add_u32 s100, s100, s89
	s_addc_u32 s101, s101, 0
	global_load_dword v65, v178, s[100:101] nt
	s_add_u32 s100, s100, s89
	s_addc_u32 s101, s101, 0
	global_load_dword v66, v178, s[100:101] nt
	s_add_u32 s100, s100, s89
	s_addc_u32 s101, s101, 0
	global_load_dword v67, v178, s[100:101] nt
	s_add_u32 s100, s100, s89
	s_addc_u32 s101, s101, 0
	global_load_dword v68, v178, s[100:101] nt
	s_add_u32 s100, s100, s89
	s_addc_u32 s101, s101, 0
	global_load_dword v69, v178, s[100:101] nt
	s_add_u32 s100, s100, s89
	s_addc_u32 s101, s101, 0
	global_load_dword v70, v178, s[100:101] nt
	s_add_u32 s100, s100, s89
	s_addc_u32 s101, s101, 0
	global_load_dword v71, v178, s[100:101] nt
	s_add_u32 s100, s100, s89
	s_addc_u32 s101, s101, 0
	global_load_dword v72, v178, s[100:101] nt
	s_add_u32 s100, s100, s89
	s_addc_u32 s101, s101, 0
	global_load_dword v73, v178, s[100:101] nt
	s_add_u32 s100, s100, s89
	s_addc_u32 s101, s101, 0
	global_load_dword v74, v178, s[100:101] nt
	s_add_u32 s100, s100, s89
	s_addc_u32 s101, s101, 0
	global_load_dword v75, v178, s[100:101] nt
	s_add_u32 s100, s100, s89
	s_addc_u32 s101, s101, 0
	global_load_dword v76, v178, s[100:101] nt
	s_add_u32 s100, s100, s89
	s_addc_u32 s101, s101, 0
	global_load_dword v77, v178, s[100:101] nt
	s_add_u32 s100, s100, s89
	s_addc_u32 s101, s101, 0
	global_load_dword v78, v178, s[100:101] nt
	s_add_u32 s100, s100, s89
	s_addc_u32 s101, s101, 0
	global_load_dword v79, v178, s[100:101] nt
	s_add_u32 s100, s100, s89
	s_addc_u32 s101, s101, 0
	global_load_dword v80, v178, s[100:101] nt
	s_add_u32 s100, s100, s89
	s_addc_u32 s101, s101, 0
	global_load_dword v81, v178, s[100:101] nt
	s_add_u32 s100, s100, s89
	s_addc_u32 s101, s101, 0
	global_load_dword v82, v178, s[100:101] nt
	s_add_u32 s100, s100, s89
	s_addc_u32 s101, s101, 0
	global_load_dword v83, v178, s[100:101] nt
	s_add_u32 s100, s100, s89
	s_addc_u32 s101, s101, 0
	global_load_dword v84, v178, s[100:101] nt
	s_add_u32 s100, s100, s89
	s_addc_u32 s101, s101, 0
	global_load_dword v85, v178, s[100:101] nt
	s_add_u32 s100, s100, s89
	s_addc_u32 s101, s101, 0
	global_load_dword v86, v178, s[100:101] nt
	s_add_u32 s100, s100, s89
	s_addc_u32 s101, s101, 0
	global_load_dword v87, v178, s[100:101] nt
	s_add_u32 s100, s100, s89
	s_addc_u32 s101, s101, 0
	global_load_dword v88, v178, s[100:101] nt
	s_add_u32 s100, s100, s89
	s_addc_u32 s101, s101, 0
	global_load_dword v89, v178, s[100:101] nt
	s_add_u32 s100, s100, s89
	s_addc_u32 s101, s101, 0
	global_load_dword v90, v178, s[100:101] nt
	s_add_u32 s100, s100, s89
	s_addc_u32 s101, s101, 0
	global_load_dword v91, v178, s[100:101] nt
	s_add_u32 s100, s100, s89
	s_addc_u32 s101, s101, 0
	global_load_dword v92, v178, s[100:101] nt
	s_add_u32 s100, s100, s89
	s_addc_u32 s101, s101, 0
	global_load_dword v93, v178, s[100:101] nt
	s_add_u32 s100, s100, s89
	s_addc_u32 s101, s101, 0
	global_load_dword v94, v178, s[100:101] nt
	s_add_u32 s100, s100, s89
	s_addc_u32 s101, s101, 0
	global_load_dword v95, v178, s[100:101] nt
	s_add_u32 s100, s100, s89
	s_addc_u32 s101, s101, 0
	global_load_dword v96, v178, s[100:101] nt
	s_add_u32 s100, s100, s89
	s_addc_u32 s101, s101, 0
	global_load_dword v97, v178, s[100:101] nt
	s_add_u32 s100, s100, s89
	s_addc_u32 s101, s101, 0
	s_waitcnt vmcnt(48)
	v_mul_f32_e32 v34, 0x42000000, v34
	v_mul_f32_e32 v35, 0x42000000, v35
	v_mul_f32_e32 v36, 0x42000000, v36
	v_mul_f32_e32 v37, 0x42000000, v37
	v_mul_f32_e32 v38, 0x42000000, v38
	v_mul_f32_e32 v39, 0x42000000, v39
	v_mul_f32_e32 v40, 0x42000000, v40
	v_mul_f32_e32 v41, 0x42000000, v41
	v_mul_f32_e32 v42, 0x42000000, v42
	v_mul_f32_e32 v43, 0x42000000, v43
	v_mul_f32_e32 v44, 0x42000000, v44
	v_mul_f32_e32 v45, 0x42000000, v45
	v_mul_f32_e32 v46, 0x42000000, v46
	v_mul_f32_e32 v47, 0x42000000, v47
	v_mul_f32_e32 v48, 0x42000000, v48
	v_mul_f32_e32 v49, 0x42000000, v49
	v_cvt_pk_fp8_f32 v154, v34, v35
	v_cvt_pk_fp8_f32 v155, v38, v39
	v_cvt_pk_fp8_f32 v156, v42, v43
	v_cvt_pk_fp8_f32 v157, v46, v47
	v_cvt_pk_fp8_f32 v154, v36, v37 op_sel:[0,0,1]
	v_cvt_pk_fp8_f32 v155, v40, v41 op_sel:[0,0,1]
	v_cvt_pk_fp8_f32 v156, v44, v45 op_sel:[0,0,1]
	v_cvt_pk_fp8_f32 v157, v48, v49 op_sel:[0,0,1]
	s_waitcnt vmcnt(32)
	v_mul_f32_e32 v50, 0x42000000, v50
	v_mul_f32_e32 v51, 0x42000000, v51
	v_mul_f32_e32 v52, 0x42000000, v52
	v_mul_f32_e32 v53, 0x42000000, v53
	v_mul_f32_e32 v54, 0x42000000, v54
	v_mul_f32_e32 v55, 0x42000000, v55
	v_mul_f32_e32 v56, 0x42000000, v56
	v_mul_f32_e32 v57, 0x42000000, v57
	v_mul_f32_e32 v58, 0x42000000, v58
	v_mul_f32_e32 v59, 0x42000000, v59
	v_mul_f32_e32 v60, 0x42000000, v60
	v_mul_f32_e32 v61, 0x42000000, v61
	v_mul_f32_e32 v62, 0x42000000, v62
	v_mul_f32_e32 v63, 0x42000000, v63
	v_mul_f32_e32 v64, 0x42000000, v64
	v_mul_f32_e32 v65, 0x42000000, v65
	v_cvt_pk_fp8_f32 v158, v50, v51
	v_cvt_pk_fp8_f32 v159, v54, v55
	v_cvt_pk_fp8_f32 v160, v58, v59
	v_cvt_pk_fp8_f32 v161, v62, v63
	v_cvt_pk_fp8_f32 v158, v52, v53 op_sel:[0,0,1]
	v_cvt_pk_fp8_f32 v159, v56, v57 op_sel:[0,0,1]
	v_cvt_pk_fp8_f32 v160, v60, v61 op_sel:[0,0,1]
	v_cvt_pk_fp8_f32 v161, v64, v65 op_sel:[0,0,1]
	s_waitcnt vmcnt(16)
	v_mul_f32_e32 v66, 0x42000000, v66
	v_mul_f32_e32 v67, 0x42000000, v67
	v_mul_f32_e32 v68, 0x42000000, v68
	v_mul_f32_e32 v69, 0x42000000, v69
	v_mul_f32_e32 v70, 0x42000000, v70
	v_mul_f32_e32 v71, 0x42000000, v71
	v_mul_f32_e32 v72, 0x42000000, v72
	v_mul_f32_e32 v73, 0x42000000, v73
	v_mul_f32_e32 v74, 0x42000000, v74
	v_mul_f32_e32 v75, 0x42000000, v75
	v_mul_f32_e32 v76, 0x42000000, v76
	v_mul_f32_e32 v77, 0x42000000, v77
	v_mul_f32_e32 v78, 0x42000000, v78
	v_mul_f32_e32 v79, 0x42000000, v79
	v_mul_f32_e32 v80, 0x42000000, v80
	v_mul_f32_e32 v81, 0x42000000, v81
	v_cvt_pk_fp8_f32 v162, v66, v67
	v_cvt_pk_fp8_f32 v163, v70, v71
	v_cvt_pk_fp8_f32 v164, v74, v75
	v_cvt_pk_fp8_f32 v165, v78, v79
	v_cvt_pk_fp8_f32 v162, v68, v69 op_sel:[0,0,1]
	v_cvt_pk_fp8_f32 v163, v72, v73 op_sel:[0,0,1]
	v_cvt_pk_fp8_f32 v164, v76, v77 op_sel:[0,0,1]
	v_cvt_pk_fp8_f32 v165, v80, v81 op_sel:[0,0,1]
	s_waitcnt vmcnt(0)
	v_mul_f32_e32 v82, 0x42000000, v82
	v_mul_f32_e32 v83, 0x42000000, v83
	v_mul_f32_e32 v84, 0x42000000, v84
	v_mul_f32_e32 v85, 0x42000000, v85
	v_mul_f32_e32 v86, 0x42000000, v86
	v_mul_f32_e32 v87, 0x42000000, v87
	v_mul_f32_e32 v88, 0x42000000, v88
	v_mul_f32_e32 v89, 0x42000000, v89
	v_mul_f32_e32 v90, 0x42000000, v90
	v_mul_f32_e32 v91, 0x42000000, v91
	v_mul_f32_e32 v92, 0x42000000, v92
	v_mul_f32_e32 v93, 0x42000000, v93
	v_mul_f32_e32 v94, 0x42000000, v94
	v_mul_f32_e32 v95, 0x42000000, v95
	v_mul_f32_e32 v96, 0x42000000, v96
	v_mul_f32_e32 v97, 0x42000000, v97
	v_cvt_pk_fp8_f32 v166, v82, v83
	v_cvt_pk_fp8_f32 v167, v86, v87
	v_cvt_pk_fp8_f32 v168, v90, v91
	v_cvt_pk_fp8_f32 v169, v94, v95
	v_cvt_pk_fp8_f32 v166, v84, v85 op_sel:[0,0,1]
	v_cvt_pk_fp8_f32 v167, v88, v89 op_sel:[0,0,1]
	v_cvt_pk_fp8_f32 v168, v92, v93 op_sel:[0,0,1]
	v_cvt_pk_fp8_f32 v169, v96, v97 op_sel:[0,0,1]
	s_mov_b32 vcc_lo, 0xaaaaaaaa
	s_mov_b32 vcc_hi, 0xaaaaaaaa
	s_nop 1
	v_cndmask_b32_dpp v170, v154, v158, vcc quad_perm:[1,0,3,2] row_mask:0xf bank_mask:0xf
	v_cndmask_b32_dpp v174, v162, v166, vcc quad_perm:[1,0,3,2] row_mask:0xf bank_mask:0xf
	v_cndmask_b32_dpp v171, v155, v159, vcc quad_perm:[1,0,3,2] row_mask:0xf bank_mask:0xf
	v_cndmask_b32_dpp v175, v163, v167, vcc quad_perm:[1,0,3,2] row_mask:0xf bank_mask:0xf
	v_cndmask_b32_dpp v172, v156, v160, vcc quad_perm:[1,0,3,2] row_mask:0xf bank_mask:0xf
	v_cndmask_b32_dpp v176, v164, v168, vcc quad_perm:[1,0,3,2] row_mask:0xf bank_mask:0xf
	v_cndmask_b32_dpp v173, v157, v161, vcc quad_perm:[1,0,3,2] row_mask:0xf bank_mask:0xf
	v_cndmask_b32_dpp v177, v165, v169, vcc quad_perm:[1,0,3,2] row_mask:0xf bank_mask:0xf
	s_mov_b32 vcc_lo, 0x55555555
	s_mov_b32 vcc_hi, 0x55555555
	s_nop 1
	v_cndmask_b32_dpp v154, v158, v154, vcc quad_perm:[1,0,3,2] row_mask:0xf bank_mask:0xf
	v_cndmask_b32_dpp v162, v166, v162, vcc quad_perm:[1,0,3,2] row_mask:0xf bank_mask:0xf
	v_cndmask_b32_dpp v155, v159, v155, vcc quad_perm:[1,0,3,2] row_mask:0xf bank_mask:0xf
	v_cndmask_b32_dpp v163, v167, v163, vcc quad_perm:[1,0,3,2] row_mask:0xf bank_mask:0xf
	v_cndmask_b32_dpp v156, v160, v156, vcc quad_perm:[1,0,3,2] row_mask:0xf bank_mask:0xf
	v_cndmask_b32_dpp v164, v168, v164, vcc quad_perm:[1,0,3,2] row_mask:0xf bank_mask:0xf
	v_cndmask_b32_dpp v157, v161, v157, vcc quad_perm:[1,0,3,2] row_mask:0xf bank_mask:0xf
	v_cndmask_b32_dpp v165, v169, v165, vcc quad_perm:[1,0,3,2] row_mask:0xf bank_mask:0xf
	s_mov_b32 vcc_lo, 0xcccccccc
	s_mov_b32 vcc_hi, 0xcccccccc
	s_nop 1
	v_cndmask_b32_dpp v158, v154, v162, vcc quad_perm:[2,3,0,1] row_mask:0xf bank_mask:0xf
	v_cndmask_b32_dpp v166, v170, v174, vcc quad_perm:[2,3,0,1] row_mask:0xf bank_mask:0xf
	v_cndmask_b32_dpp v159, v155, v163, vcc quad_perm:[2,3,0,1] row_mask:0xf bank_mask:0xf
	v_cndmask_b32_dpp v167, v171, v175, vcc quad_perm:[2,3,0,1] row_mask:0xf bank_mask:0xf
	v_cndmask_b32_dpp v160, v156, v164, vcc quad_perm:[2,3,0,1] row_mask:0xf bank_mask:0xf
	v_cndmask_b32_dpp v168, v172, v176, vcc quad_perm:[2,3,0,1] row_mask:0xf bank_mask:0xf
	v_cndmask_b32_dpp v161, v157, v165, vcc quad_perm:[2,3,0,1] row_mask:0xf bank_mask:0xf
	v_cndmask_b32_dpp v169, v173, v177, vcc quad_perm:[2,3,0,1] row_mask:0xf bank_mask:0xf
	s_mov_b32 vcc_lo, 0x33333333
	s_mov_b32 vcc_hi, 0x33333333
	s_nop 1
	v_cndmask_b32_dpp v154, v162, v154, vcc quad_perm:[2,3,0,1] row_mask:0xf bank_mask:0xf
	v_cndmask_b32_dpp v170, v174, v170, vcc quad_perm:[2,3,0,1] row_mask:0xf bank_mask:0xf
	v_cndmask_b32_dpp v155, v163, v155, vcc quad_perm:[2,3,0,1] row_mask:0xf bank_mask:0xf
	v_cndmask_b32_dpp v171, v175, v171, vcc quad_perm:[2,3,0,1] row_mask:0xf bank_mask:0xf
	v_cndmask_b32_dpp v156, v164, v156, vcc quad_perm:[2,3,0,1] row_mask:0xf bank_mask:0xf
	v_cndmask_b32_dpp v172, v176, v172, vcc quad_perm:[2,3,0,1] row_mask:0xf bank_mask:0xf
	v_cndmask_b32_dpp v157, v165, v157, vcc quad_perm:[2,3,0,1] row_mask:0xf bank_mask:0xf
	v_cndmask_b32_dpp v173, v177, v173, vcc quad_perm:[2,3,0,1] row_mask:0xf bank_mask:0xf
	global_store_dwordx4 v179, v[154:157], s[82:83]
	global_store_dwordx4 v180, v[170:173], s[82:83]
	global_store_dwordx4 v181, v[158:161], s[82:83]
	global_store_dwordx4 v190, v[166:169], s[82:83]
	v_readlane_b32 s2, v239, 0
	s_lshr_b32 s2, s2, 6
	s_add_i32 s2, s2, 6
	s_cmp_gt_u32 s2, 13
	s_cbranch_scc1 .Lhw_seam3_done
	s_add_i32 s2, s2, 42
	s_mul_i32 s2, s2, s74
	v_readlane_b32 s9, v239, 23
	s_lshr_b32 s9, s9, 3
	s_add_i32 s2, s2, s9
	s_cmp_gt_u32 s2, 24575
	s_cbranch_scc1 .Lhw_seam3_done
	v_mbcnt_lo_u32_b32 v178, -1, 0
	v_mbcnt_hi_u32_b32 v178, -1, v178
	v_and_b32_e32 v179, 60, v178
	v_lshlrev_b32_e32 v179, 10, v179
	v_and_b32_e32 v180, 3, v178
	v_lshl_or_b32 v179, v180, 4, v179
	v_add_u32_e32 v180, 0x400, v179
	v_add_u32_e32 v181, 0x800, v179
	v_add_u32_e32 v190, 0xc00, v179
	v_lshlrev_b32_e32 v178, 2, v178
	s_cmp_lt_u32 s2, 16384
	s_cbranch_scc0 .Lhw_dn_s3_1
	s_lshr_b32 s9, s2, 9
	s_bfe_u32 s32, s2, 0x40005
	s_and_b32 s53, s2, 31
	s_lshl_b32 s69, s9, 23
	s_lshl_b32 s100, s32, 19
	s_add_i32 s69, s69, s100
	s_lshl_b32 s100, s53, 8
	s_add_i32 s69, s69, s100
	s_lshl_b32 s98, s9, 11
	s_bfe_u32 s100, s53, 0x30001
	s_lshl_b32 s100, s100, 8
	s_add_i32 s98, s98, s100
	s_lshr_b32 s100, s53, 4
	s_lshl_b32 s100, s100, 7
	s_add_i32 s98, s98, s100
	s_and_b32 s100, s53, 1
	s_lshl_b32 s100, s100, 6
	s_add_i32 s98, s98, s100
	s_lshl_b32 s98, s98, 10
	s_lshl_b32 s100, s32, 6
	s_add_i32 s98, s98, s100
	s_add_i32 s98, s98, 0x2000000
	v_readlane_b32 s82, v239, 11
	v_readlane_b32 s83, v239, 12
	s_movk_i32 s89, 8192
	s_branch .Lhw_go_s3_1

.Lhw_go_s4_0:
	s_add_u32 s100, s82, s69
	s_addc_u32 s101, s83, 0
	v_readlane_b32 s82, v239, 44
	v_readlane_b32 s83, v239, 45
	s_add_u32 s82, s82, s98
	s_addc_u32 s83, s83, 0
	global_load_dword v34, v178, s[100:101] nt
	s_add_u32 s100, s100, s89
	s_addc_u32 s101, s101, 0
	global_load_dword v35, v178, s[100:101] nt
	s_add_u32 s100, s100, s89
	s_addc_u32 s101, s101, 0
	global_load_dword v36, v178, s[100:101] nt
	s_add_u32 s100, s100, s89
	s_addc_u32 s101, s101, 0
	global_load_dword v37, v178, s[100:101] nt
	s_add_u32 s100, s100, s89
	s_addc_u32 s101, s101, 0
	global_load_dword v38, v178, s[100:101] nt
	s_add_u32 s100, s100, s89
	s_addc_u32 s101, s101, 0
	global_load_dword v39, v178, s[100:101] nt
	s_add_u32 s100, s100, s89
	s_addc_u32 s101, s101, 0
	global_load_dword v40, v178, s[100:101] nt
	s_add_u32 s100, s100, s89
	s_addc_u32 s101, s101, 0
	global_load_dword v41, v178, s[100:101] nt
	s_add_u32 s100, s100, s89
	s_addc_u32 s101, s101, 0
	global_load_dword v42, v178, s[100:101] nt
	s_add_u32 s100, s100, s89
	s_addc_u32 s101, s101, 0
	global_load_dword v43, v178, s[100:101] nt
	s_add_u32 s100, s100, s89
	s_addc_u32 s101, s101, 0
	global_load_dword v44, v178, s[100:101] nt
	s_add_u32 s100, s100, s89
	s_addc_u32 s101, s101, 0
	global_load_dword v45, v178, s[100:101] nt
	s_add_u32 s100, s100, s89
	s_addc_u32 s101, s101, 0
	global_load_dword v46, v178, s[100:101] nt
	s_add_u32 s100, s100, s89
	s_addc_u32 s101, s101, 0
	global_load_dword v47, v178, s[100:101] nt
	s_add_u32 s100, s100, s89
	s_addc_u32 s101, s101, 0
	global_load_dword v48, v178, s[100:101] nt
	s_add_u32 s100, s100, s89
	s_addc_u32 s101, s101, 0
	global_load_dword v49, v178, s[100:101] nt
	s_add_u32 s100, s100, s89
	s_addc_u32 s101, s101, 0
	global_load_dword v50, v178, s[100:101] nt
	s_add_u32 s100, s100, s89
	s_addc_u32 s101, s101, 0
	global_load_dword v51, v178, s[100:101] nt
	s_add_u32 s100, s100, s89
	s_addc_u32 s101, s101, 0
	global_load_dword v52, v178, s[100:101] nt
	s_add_u32 s100, s100, s89
	s_addc_u32 s101, s101, 0
	global_load_dword v53, v178, s[100:101] nt
	s_add_u32 s100, s100, s89
	s_addc_u32 s101, s101, 0
	global_load_dword v54, v178, s[100:101] nt
	s_add_u32 s100, s100, s89
	s_addc_u32 s101, s101, 0
	global_load_dword v55, v178, s[100:101] nt
	s_add_u32 s100, s100, s89
	s_addc_u32 s101, s101, 0
	global_load_dword v56, v178, s[100:101] nt
	s_add_u32 s100, s100, s89
	s_addc_u32 s101, s101, 0
	global_load_dword v57, v178, s[100:101] nt
	s_add_u32 s100, s100, s89
	s_addc_u32 s101, s101, 0
	global_load_dword v58, v178, s[100:101] nt
	s_add_u32 s100, s100, s89
	s_addc_u32 s101, s101, 0
	global_load_dword v59, v178, s[100:101] nt
	s_add_u32 s100, s100, s89
	s_addc_u32 s101, s101, 0
	global_load_dword v60, v178, s[100:101] nt
	s_add_u32 s100, s100, s89
	s_addc_u32 s101, s101, 0
	global_load_dword v61, v178, s[100:101] nt
	s_add_u32 s100, s100, s89
	s_addc_u32 s101, s101, 0
	global_load_dword v62, v178, s[100:101] nt
	s_add_u32 s100, s100, s89
	s_addc_u32 s101, s101, 0
	global_load_dword v63, v178, s[100:101] nt
	s_add_u32 s100, s100, s89
	s_addc_u32 s101, s101, 0
	global_load_dword v64, v178, s[100:101] nt
	s_add_u32 s100, s100, s89
	s_addc_u32 s101, s101, 0
	global_load_dword v65, v178, s[100:101] nt
	s_add_u32 s100, s100, s89
	s_addc_u32 s101, s101, 0
	global_load_dword v66, v178, s[100:101] nt
	s_add_u32 s100, s100, s89
	s_addc_u32 s101, s101, 0
	global_load_dword v67, v178, s[100:101] nt
	s_add_u32 s100, s100, s89
	s_addc_u32 s101, s101, 0
	global_load_dword v68, v178, s[100:101] nt
	s_add_u32 s100, s100, s89
	s_addc_u32 s101, s101, 0
	global_load_dword v69, v178, s[100:101] nt
	s_add_u32 s100, s100, s89
	s_addc_u32 s101, s101, 0
	global_load_dword v70, v178, s[100:101] nt
	s_add_u32 s100, s100, s89
	s_addc_u32 s101, s101, 0
	global_load_dword v71, v178, s[100:101] nt
	s_add_u32 s100, s100, s89
	s_addc_u32 s101, s101, 0
	global_load_dword v72, v178, s[100:101] nt
	s_add_u32 s100, s100, s89
	s_addc_u32 s101, s101, 0
	global_load_dword v73, v178, s[100:101] nt
	s_add_u32 s100, s100, s89
	s_addc_u32 s101, s101, 0
	global_load_dword v74, v178, s[100:101] nt
	s_add_u32 s100, s100, s89
	s_addc_u32 s101, s101, 0
	global_load_dword v75, v178, s[100:101] nt
	s_add_u32 s100, s100, s89
	s_addc_u32 s101, s101, 0
	global_load_dword v76, v178, s[100:101] nt
	s_add_u32 s100, s100, s89
	s_addc_u32 s101, s101, 0
	global_load_dword v77, v178, s[100:101] nt
	s_add_u32 s100, s100, s89
	s_addc_u32 s101, s101, 0
	global_load_dword v78, v178, s[100:101] nt
	s_add_u32 s100, s100, s89
	s_addc_u32 s101, s101, 0
	global_load_dword v79, v178, s[100:101] nt
	s_add_u32 s100, s100, s89
	s_addc_u32 s101, s101, 0
	global_load_dword v80, v178, s[100:101] nt
	s_add_u32 s100, s100, s89
	s_addc_u32 s101, s101, 0
	global_load_dword v81, v178, s[100:101] nt
	s_add_u32 s100, s100, s89
	s_addc_u32 s101, s101, 0
	global_load_dword v82, v178, s[100:101] nt
	s_add_u32 s100, s100, s89
	s_addc_u32 s101, s101, 0
	global_load_dword v83, v178, s[100:101] nt
	s_add_u32 s100, s100, s89
	s_addc_u32 s101, s101, 0
	global_load_dword v84, v178, s[100:101] nt
	s_add_u32 s100, s100, s89
	s_addc_u32 s101, s101, 0
	global_load_dword v85, v178, s[100:101] nt
	s_add_u32 s100, s100, s89
	s_addc_u32 s101, s101, 0
	global_load_dword v86, v178, s[100:101] nt
	s_add_u32 s100, s100, s89
	s_addc_u32 s101, s101, 0
	global_load_dword v87, v178, s[100:101] nt
	s_add_u32 s100, s100, s89
	s_addc_u32 s101, s101, 0
	global_load_dword v88, v178, s[100:101] nt
	s_add_u32 s100, s100, s89
	s_addc_u32 s101, s101, 0
	global_load_dword v89, v178, s[100:101] nt
	s_add_u32 s100, s100, s89
	s_addc_u32 s101, s101, 0
	global_load_dword v90, v178, s[100:101] nt
	s_add_u32 s100, s100, s89
	s_addc_u32 s101, s101, 0
	global_load_dword v91, v178, s[100:101] nt
	s_add_u32 s100, s100, s89
	s_addc_u32 s101, s101, 0
	global_load_dword v92, v178, s[100:101] nt
	s_add_u32 s100, s100, s89
	s_addc_u32 s101, s101, 0
	global_load_dword v93, v178, s[100:101] nt
	s_add_u32 s100, s100, s89
	s_addc_u32 s101, s101, 0
	global_load_dword v94, v178, s[100:101] nt
	s_add_u32 s100, s100, s89
	s_addc_u32 s101, s101, 0
	global_load_dword v95, v178, s[100:101] nt
	s_add_u32 s100, s100, s89
	s_addc_u32 s101, s101, 0
	global_load_dword v96, v178, s[100:101] nt
	s_add_u32 s100, s100, s89
	s_addc_u32 s101, s101, 0
	global_load_dword v97, v178, s[100:101] nt
	s_add_u32 s100, s100, s89
	s_addc_u32 s101, s101, 0
	s_waitcnt vmcnt(48)
	v_mul_f32_e32 v34, 0x42000000, v34
	v_mul_f32_e32 v35, 0x42000000, v35
	v_mul_f32_e32 v36, 0x42000000, v36
	v_mul_f32_e32 v37, 0x42000000, v37
	v_mul_f32_e32 v38, 0x42000000, v38
	v_mul_f32_e32 v39, 0x42000000, v39
	v_mul_f32_e32 v40, 0x42000000, v40
	v_mul_f32_e32 v41, 0x42000000, v41
	v_mul_f32_e32 v42, 0x42000000, v42
	v_mul_f32_e32 v43, 0x42000000, v43
	v_mul_f32_e32 v44, 0x42000000, v44
	v_mul_f32_e32 v45, 0x42000000, v45
	v_mul_f32_e32 v46, 0x42000000, v46
	v_mul_f32_e32 v47, 0x42000000, v47
	v_mul_f32_e32 v48, 0x42000000, v48
	v_mul_f32_e32 v49, 0x42000000, v49
	v_cvt_pk_fp8_f32 v154, v34, v35
	v_cvt_pk_fp8_f32 v155, v38, v39
	v_cvt_pk_fp8_f32 v156, v42, v43
	v_cvt_pk_fp8_f32 v157, v46, v47
	v_cvt_pk_fp8_f32 v154, v36, v37 op_sel:[0,0,1]
	v_cvt_pk_fp8_f32 v155, v40, v41 op_sel:[0,0,1]
	v_cvt_pk_fp8_f32 v156, v44, v45 op_sel:[0,0,1]
	v_cvt_pk_fp8_f32 v157, v48, v49 op_sel:[0,0,1]
	s_waitcnt vmcnt(32)
	v_mul_f32_e32 v50, 0x42000000, v50
	v_mul_f32_e32 v51, 0x42000000, v51
	v_mul_f32_e32 v52, 0x42000000, v52
	v_mul_f32_e32 v53, 0x42000000, v53
	v_mul_f32_e32 v54, 0x42000000, v54
	v_mul_f32_e32 v55, 0x42000000, v55
	v_mul_f32_e32 v56, 0x42000000, v56
	v_mul_f32_e32 v57, 0x42000000, v57
	v_mul_f32_e32 v58, 0x42000000, v58
	v_mul_f32_e32 v59, 0x42000000, v59
	v_mul_f32_e32 v60, 0x42000000, v60
	v_mul_f32_e32 v61, 0x42000000, v61
	v_mul_f32_e32 v62, 0x42000000, v62
	v_mul_f32_e32 v63, 0x42000000, v63
	v_mul_f32_e32 v64, 0x42000000, v64
	v_mul_f32_e32 v65, 0x42000000, v65
	v_cvt_pk_fp8_f32 v158, v50, v51
	v_cvt_pk_fp8_f32 v159, v54, v55
	v_cvt_pk_fp8_f32 v160, v58, v59
	v_cvt_pk_fp8_f32 v161, v62, v63
	v_cvt_pk_fp8_f32 v158, v52, v53 op_sel:[0,0,1]
	v_cvt_pk_fp8_f32 v159, v56, v57 op_sel:[0,0,1]
	v_cvt_pk_fp8_f32 v160, v60, v61 op_sel:[0,0,1]
	v_cvt_pk_fp8_f32 v161, v64, v65 op_sel:[0,0,1]
	s_waitcnt vmcnt(16)
	v_mul_f32_e32 v66, 0x42000000, v66
	v_mul_f32_e32 v67, 0x42000000, v67
	v_mul_f32_e32 v68, 0x42000000, v68
	v_mul_f32_e32 v69, 0x42000000, v69
	v_mul_f32_e32 v70, 0x42000000, v70
	v_mul_f32_e32 v71, 0x42000000, v71
	v_mul_f32_e32 v72, 0x42000000, v72
	v_mul_f32_e32 v73, 0x42000000, v73
	v_mul_f32_e32 v74, 0x42000000, v74
	v_mul_f32_e32 v75, 0x42000000, v75
	v_mul_f32_e32 v76, 0x42000000, v76
	v_mul_f32_e32 v77, 0x42000000, v77
	v_mul_f32_e32 v78, 0x42000000, v78
	v_mul_f32_e32 v79, 0x42000000, v79
	v_mul_f32_e32 v80, 0x42000000, v80
	v_mul_f32_e32 v81, 0x42000000, v81
	v_cvt_pk_fp8_f32 v162, v66, v67
	v_cvt_pk_fp8_f32 v163, v70, v71
	v_cvt_pk_fp8_f32 v164, v74, v75
	v_cvt_pk_fp8_f32 v165, v78, v79
	v_cvt_pk_fp8_f32 v162, v68, v69 op_sel:[0,0,1]
	v_cvt_pk_fp8_f32 v163, v72, v73 op_sel:[0,0,1]
	v_cvt_pk_fp8_f32 v164, v76, v77 op_sel:[0,0,1]
	v_cvt_pk_fp8_f32 v165, v80, v81 op_sel:[0,0,1]
	s_waitcnt vmcnt(0)
	v_mul_f32_e32 v82, 0x42000000, v82
	v_mul_f32_e32 v83, 0x42000000, v83
	v_mul_f32_e32 v84, 0x42000000, v84
	v_mul_f32_e32 v85, 0x42000000, v85
	v_mul_f32_e32 v86, 0x42000000, v86
	v_mul_f32_e32 v87, 0x42000000, v87
	v_mul_f32_e32 v88, 0x42000000, v88
	v_mul_f32_e32 v89, 0x42000000, v89
	v_mul_f32_e32 v90, 0x42000000, v90
	v_mul_f32_e32 v91, 0x42000000, v91
	v_mul_f32_e32 v92, 0x42000000, v92
	v_mul_f32_e32 v93, 0x42000000, v93
	v_mul_f32_e32 v94, 0x42000000, v94
	v_mul_f32_e32 v95, 0x42000000, v95
	v_mul_f32_e32 v96, 0x42000000, v96
	v_mul_f32_e32 v97, 0x42000000, v97
	v_cvt_pk_fp8_f32 v166, v82, v83
	v_cvt_pk_fp8_f32 v167, v86, v87
	v_cvt_pk_fp8_f32 v168, v90, v91
	v_cvt_pk_fp8_f32 v169, v94, v95
	v_cvt_pk_fp8_f32 v166, v84, v85 op_sel:[0,0,1]
	v_cvt_pk_fp8_f32 v167, v88, v89 op_sel:[0,0,1]
	v_cvt_pk_fp8_f32 v168, v92, v93 op_sel:[0,0,1]
	v_cvt_pk_fp8_f32 v169, v96, v97 op_sel:[0,0,1]
	s_mov_b32 vcc_lo, 0xaaaaaaaa
	s_mov_b32 vcc_hi, 0xaaaaaaaa
	s_nop 1
	v_cndmask_b32_dpp v170, v154, v158, vcc quad_perm:[1,0,3,2] row_mask:0xf bank_mask:0xf
	v_cndmask_b32_dpp v174, v162, v166, vcc quad_perm:[1,0,3,2] row_mask:0xf bank_mask:0xf
	v_cndmask_b32_dpp v171, v155, v159, vcc quad_perm:[1,0,3,2] row_mask:0xf bank_mask:0xf
	v_cndmask_b32_dpp v175, v163, v167, vcc quad_perm:[1,0,3,2] row_mask:0xf bank_mask:0xf
	v_cndmask_b32_dpp v172, v156, v160, vcc quad_perm:[1,0,3,2] row_mask:0xf bank_mask:0xf
	v_cndmask_b32_dpp v176, v164, v168, vcc quad_perm:[1,0,3,2] row_mask:0xf bank_mask:0xf
	v_cndmask_b32_dpp v173, v157, v161, vcc quad_perm:[1,0,3,2] row_mask:0xf bank_mask:0xf
	v_cndmask_b32_dpp v177, v165, v169, vcc quad_perm:[1,0,3,2] row_mask:0xf bank_mask:0xf
	s_mov_b32 vcc_lo, 0x55555555
	s_mov_b32 vcc_hi, 0x55555555
	s_nop 1
	v_cndmask_b32_dpp v154, v158, v154, vcc quad_perm:[1,0,3,2] row_mask:0xf bank_mask:0xf
	v_cndmask_b32_dpp v162, v166, v162, vcc quad_perm:[1,0,3,2] row_mask:0xf bank_mask:0xf
	v_cndmask_b32_dpp v155, v159, v155, vcc quad_perm:[1,0,3,2] row_mask:0xf bank_mask:0xf
	v_cndmask_b32_dpp v163, v167, v163, vcc quad_perm:[1,0,3,2] row_mask:0xf bank_mask:0xf
	v_cndmask_b32_dpp v156, v160, v156, vcc quad_perm:[1,0,3,2] row_mask:0xf bank_mask:0xf
	v_cndmask_b32_dpp v164, v168, v164, vcc quad_perm:[1,0,3,2] row_mask:0xf bank_mask:0xf
	v_cndmask_b32_dpp v157, v161, v157, vcc quad_perm:[1,0,3,2] row_mask:0xf bank_mask:0xf
	v_cndmask_b32_dpp v165, v169, v165, vcc quad_perm:[1,0,3,2] row_mask:0xf bank_mask:0xf
	s_mov_b32 vcc_lo, 0xcccccccc
	s_mov_b32 vcc_hi, 0xcccccccc
	s_nop 1
	v_cndmask_b32_dpp v158, v154, v162, vcc quad_perm:[2,3,0,1] row_mask:0xf bank_mask:0xf
	v_cndmask_b32_dpp v166, v170, v174, vcc quad_perm:[2,3,0,1] row_mask:0xf bank_mask:0xf
	v_cndmask_b32_dpp v159, v155, v163, vcc quad_perm:[2,3,0,1] row_mask:0xf bank_mask:0xf
	v_cndmask_b32_dpp v167, v171, v175, vcc quad_perm:[2,3,0,1] row_mask:0xf bank_mask:0xf
	v_cndmask_b32_dpp v160, v156, v164, vcc quad_perm:[2,3,0,1] row_mask:0xf bank_mask:0xf
	v_cndmask_b32_dpp v168, v172, v176, vcc quad_perm:[2,3,0,1] row_mask:0xf bank_mask:0xf
	v_cndmask_b32_dpp v161, v157, v165, vcc quad_perm:[2,3,0,1] row_mask:0xf bank_mask:0xf
	v_cndmask_b32_dpp v169, v173, v177, vcc quad_perm:[2,3,0,1] row_mask:0xf bank_mask:0xf
	s_mov_b32 vcc_lo, 0x33333333
	s_mov_b32 vcc_hi, 0x33333333
	s_nop 1
	v_cndmask_b32_dpp v154, v162, v154, vcc quad_perm:[2,3,0,1] row_mask:0xf bank_mask:0xf
	v_cndmask_b32_dpp v170, v174, v170, vcc quad_perm:[2,3,0,1] row_mask:0xf bank_mask:0xf
	v_cndmask_b32_dpp v155, v163, v155, vcc quad_perm:[2,3,0,1] row_mask:0xf bank_mask:0xf
	v_cndmask_b32_dpp v171, v175, v171, vcc quad_perm:[2,3,0,1] row_mask:0xf bank_mask:0xf
	v_cndmask_b32_dpp v156, v164, v156, vcc quad_perm:[2,3,0,1] row_mask:0xf bank_mask:0xf
	v_cndmask_b32_dpp v172, v176, v172, vcc quad_perm:[2,3,0,1] row_mask:0xf bank_mask:0xf
	v_cndmask_b32_dpp v157, v165, v157, vcc quad_perm:[2,3,0,1] row_mask:0xf bank_mask:0xf
	v_cndmask_b32_dpp v173, v177, v173, vcc quad_perm:[2,3,0,1] row_mask:0xf bank_mask:0xf
	global_store_dwordx4 v179, v[154:157], s[82:83]
	global_store_dwordx4 v180, v[170:173], s[82:83]
	global_store_dwordx4 v181, v[158:161], s[82:83]
	global_store_dwordx4 v190, v[166:169], s[82:83]
	v_readlane_b32 s2, v239, 0
	s_lshr_b32 s2, s2, 6
	s_add_i32 s2, s2, 6
	s_cmp_gt_u32 s2, 13
	s_cbranch_scc1 .Lhw_seam4_done
	s_add_i32 s2, s2, 56
	s_mul_i32 s2, s2, s74
	v_readlane_b32 s9, v239, 23
	s_lshr_b32 s9, s9, 3
	s_add_i32 s2, s2, s9
	s_cmp_gt_u32 s2, 24575
	s_cbranch_scc1 .Lhw_seam4_done
	v_mbcnt_lo_u32_b32 v178, -1, 0
	v_mbcnt_hi_u32_b32 v178, -1, v178
	v_and_b32_e32 v179, 60, v178
	v_lshlrev_b32_e32 v179, 10, v179
	v_and_b32_e32 v180, 3, v178
	v_lshl_or_b32 v179, v180, 4, v179
	v_add_u32_e32 v180, 0x400, v179
	v_add_u32_e32 v181, 0x800, v179
	v_add_u32_e32 v190, 0xc00, v179
	v_lshlrev_b32_e32 v178, 2, v178
	s_cmp_lt_u32 s2, 16384
	s_cbranch_scc0 .Lhw_dn_s4_1
	s_lshr_b32 s9, s2, 9
	s_bfe_u32 s32, s2, 0x40005
	s_and_b32 s53, s2, 31
	s_lshl_b32 s69, s9, 23
	s_lshl_b32 s100, s32, 19
	s_add_i32 s69, s69, s100
	s_lshl_b32 s100, s53, 8
	s_add_i32 s69, s69, s100
	s_lshl_b32 s98, s9, 11
	s_bfe_u32 s100, s53, 0x30001
	s_lshl_b32 s100, s100, 8
	s_add_i32 s98, s98, s100
	s_lshr_b32 s100, s53, 4
	s_lshl_b32 s100, s100, 7
	s_add_i32 s98, s98, s100
	s_and_b32 s100, s53, 1
	s_lshl_b32 s100, s100, 6
	s_add_i32 s98, s98, s100
	s_lshl_b32 s98, s98, 10
	s_lshl_b32 s100, s32, 6
	s_add_i32 s98, s98, s100
	s_add_i32 s98, s98, 0x2000000
	v_readlane_b32 s82, v239, 11
	v_readlane_b32 s83, v239, 12
	s_movk_i32 s89, 8192
	s_branch .Lhw_go_s4_1

.Lhw_go_s5_0:
	s_add_u32 s100, s82, s69
	s_addc_u32 s101, s83, 0
	v_readlane_b32 s82, v239, 44
	v_readlane_b32 s83, v239, 45
	s_add_u32 s82, s82, s98
	s_addc_u32 s83, s83, 0
	global_load_dword v34, v178, s[100:101] nt
	s_add_u32 s100, s100, s89
	s_addc_u32 s101, s101, 0
	global_load_dword v35, v178, s[100:101] nt
	s_add_u32 s100, s100, s89
	s_addc_u32 s101, s101, 0
	global_load_dword v36, v178, s[100:101] nt
	s_add_u32 s100, s100, s89
	s_addc_u32 s101, s101, 0
	global_load_dword v37, v178, s[100:101] nt
	s_add_u32 s100, s100, s89
	s_addc_u32 s101, s101, 0
	global_load_dword v38, v178, s[100:101] nt
	s_add_u32 s100, s100, s89
	s_addc_u32 s101, s101, 0
	global_load_dword v39, v178, s[100:101] nt
	s_add_u32 s100, s100, s89
	s_addc_u32 s101, s101, 0
	global_load_dword v40, v178, s[100:101] nt
	s_add_u32 s100, s100, s89
	s_addc_u32 s101, s101, 0
	global_load_dword v41, v178, s[100:101] nt
	s_add_u32 s100, s100, s89
	s_addc_u32 s101, s101, 0
	global_load_dword v42, v178, s[100:101] nt
	s_add_u32 s100, s100, s89
	s_addc_u32 s101, s101, 0
	global_load_dword v43, v178, s[100:101] nt
	s_add_u32 s100, s100, s89
	s_addc_u32 s101, s101, 0
	global_load_dword v44, v178, s[100:101] nt
	s_add_u32 s100, s100, s89
	s_addc_u32 s101, s101, 0
	global_load_dword v45, v178, s[100:101] nt
	s_add_u32 s100, s100, s89
	s_addc_u32 s101, s101, 0
	global_load_dword v46, v178, s[100:101] nt
	s_add_u32 s100, s100, s89
	s_addc_u32 s101, s101, 0
	global_load_dword v47, v178, s[100:101] nt
	s_add_u32 s100, s100, s89
	s_addc_u32 s101, s101, 0
	global_load_dword v48, v178, s[100:101] nt
	s_add_u32 s100, s100, s89
	s_addc_u32 s101, s101, 0
	global_load_dword v49, v178, s[100:101] nt
	s_add_u32 s100, s100, s89
	s_addc_u32 s101, s101, 0
	global_load_dword v50, v178, s[100:101] nt
	s_add_u32 s100, s100, s89
	s_addc_u32 s101, s101, 0
	global_load_dword v51, v178, s[100:101] nt
	s_add_u32 s100, s100, s89
	s_addc_u32 s101, s101, 0
	global_load_dword v52, v178, s[100:101] nt
	s_add_u32 s100, s100, s89
	s_addc_u32 s101, s101, 0
	global_load_dword v53, v178, s[100:101] nt
	s_add_u32 s100, s100, s89
	s_addc_u32 s101, s101, 0
	global_load_dword v54, v178, s[100:101] nt
	s_add_u32 s100, s100, s89
	s_addc_u32 s101, s101, 0
	global_load_dword v55, v178, s[100:101] nt
	s_add_u32 s100, s100, s89
	s_addc_u32 s101, s101, 0
	global_load_dword v56, v178, s[100:101] nt
	s_add_u32 s100, s100, s89
	s_addc_u32 s101, s101, 0
	global_load_dword v57, v178, s[100:101] nt
	s_add_u32 s100, s100, s89
	s_addc_u32 s101, s101, 0
	global_load_dword v58, v178, s[100:101] nt
	s_add_u32 s100, s100, s89
	s_addc_u32 s101, s101, 0
	global_load_dword v59, v178, s[100:101] nt
	s_add_u32 s100, s100, s89
	s_addc_u32 s101, s101, 0
	global_load_dword v60, v178, s[100:101] nt
	s_add_u32 s100, s100, s89
	s_addc_u32 s101, s101, 0
	global_load_dword v61, v178, s[100:101] nt
	s_add_u32 s100, s100, s89
	s_addc_u32 s101, s101, 0
	global_load_dword v62, v178, s[100:101] nt
	s_add_u32 s100, s100, s89
	s_addc_u32 s101, s101, 0
	global_load_dword v63, v178, s[100:101] nt
	s_add_u32 s100, s100, s89
	s_addc_u32 s101, s101, 0
	global_load_dword v64, v178, s[100:101] nt
	s_add_u32 s100, s100, s89
	s_addc_u32 s101, s101, 0
	global_load_dword v65, v178, s[100:101] nt
	s_add_u32 s100, s100, s89
	s_addc_u32 s101, s101, 0
	global_load_dword v66, v178, s[100:101] nt
	s_add_u32 s100, s100, s89
	s_addc_u32 s101, s101, 0
	global_load_dword v67, v178, s[100:101] nt
	s_add_u32 s100, s100, s89
	s_addc_u32 s101, s101, 0
	global_load_dword v68, v178, s[100:101] nt
	s_add_u32 s100, s100, s89
	s_addc_u32 s101, s101, 0
	global_load_dword v69, v178, s[100:101] nt
	s_add_u32 s100, s100, s89
	s_addc_u32 s101, s101, 0
	global_load_dword v70, v178, s[100:101] nt
	s_add_u32 s100, s100, s89
	s_addc_u32 s101, s101, 0
	global_load_dword v71, v178, s[100:101] nt
	s_add_u32 s100, s100, s89
	s_addc_u32 s101, s101, 0
	global_load_dword v72, v178, s[100:101] nt
	s_add_u32 s100, s100, s89
	s_addc_u32 s101, s101, 0
	global_load_dword v73, v178, s[100:101] nt
	s_add_u32 s100, s100, s89
	s_addc_u32 s101, s101, 0
	global_load_dword v74, v178, s[100:101] nt
	s_add_u32 s100, s100, s89
	s_addc_u32 s101, s101, 0
	global_load_dword v75, v178, s[100:101] nt
	s_add_u32 s100, s100, s89
	s_addc_u32 s101, s101, 0
	global_load_dword v76, v178, s[100:101] nt
	s_add_u32 s100, s100, s89
	s_addc_u32 s101, s101, 0
	global_load_dword v77, v178, s[100:101] nt
	s_add_u32 s100, s100, s89
	s_addc_u32 s101, s101, 0
	global_load_dword v78, v178, s[100:101] nt
	s_add_u32 s100, s100, s89
	s_addc_u32 s101, s101, 0
	global_load_dword v79, v178, s[100:101] nt
	s_add_u32 s100, s100, s89
	s_addc_u32 s101, s101, 0
	global_load_dword v80, v178, s[100:101] nt
	s_add_u32 s100, s100, s89
	s_addc_u32 s101, s101, 0
	global_load_dword v81, v178, s[100:101] nt
	s_add_u32 s100, s100, s89
	s_addc_u32 s101, s101, 0
	global_load_dword v82, v178, s[100:101] nt
	s_add_u32 s100, s100, s89
	s_addc_u32 s101, s101, 0
	global_load_dword v83, v178, s[100:101] nt
	s_add_u32 s100, s100, s89
	s_addc_u32 s101, s101, 0
	global_load_dword v84, v178, s[100:101] nt
	s_add_u32 s100, s100, s89
	s_addc_u32 s101, s101, 0
	global_load_dword v85, v178, s[100:101] nt
	s_add_u32 s100, s100, s89
	s_addc_u32 s101, s101, 0
	global_load_dword v86, v178, s[100:101] nt
	s_add_u32 s100, s100, s89
	s_addc_u32 s101, s101, 0
	global_load_dword v87, v178, s[100:101] nt
	s_add_u32 s100, s100, s89
	s_addc_u32 s101, s101, 0
	global_load_dword v88, v178, s[100:101] nt
	s_add_u32 s100, s100, s89
	s_addc_u32 s101, s101, 0
	global_load_dword v89, v178, s[100:101] nt
	s_add_u32 s100, s100, s89
	s_addc_u32 s101, s101, 0
	global_load_dword v90, v178, s[100:101] nt
	s_add_u32 s100, s100, s89
	s_addc_u32 s101, s101, 0
	global_load_dword v91, v178, s[100:101] nt
	s_add_u32 s100, s100, s89
	s_addc_u32 s101, s101, 0
	global_load_dword v92, v178, s[100:101] nt
	s_add_u32 s100, s100, s89
	s_addc_u32 s101, s101, 0
	global_load_dword v93, v178, s[100:101] nt
	s_add_u32 s100, s100, s89
	s_addc_u32 s101, s101, 0
	global_load_dword v94, v178, s[100:101] nt
	s_add_u32 s100, s100, s89
	s_addc_u32 s101, s101, 0
	global_load_dword v95, v178, s[100:101] nt
	s_add_u32 s100, s100, s89
	s_addc_u32 s101, s101, 0
	global_load_dword v96, v178, s[100:101] nt
	s_add_u32 s100, s100, s89
	s_addc_u32 s101, s101, 0
	global_load_dword v97, v178, s[100:101] nt
	s_add_u32 s100, s100, s89
	s_addc_u32 s101, s101, 0
	s_waitcnt vmcnt(48)
	v_mul_f32_e32 v34, 0x42000000, v34
	v_mul_f32_e32 v35, 0x42000000, v35
	v_mul_f32_e32 v36, 0x42000000, v36
	v_mul_f32_e32 v37, 0x42000000, v37
	v_mul_f32_e32 v38, 0x42000000, v38
	v_mul_f32_e32 v39, 0x42000000, v39
	v_mul_f32_e32 v40, 0x42000000, v40
	v_mul_f32_e32 v41, 0x42000000, v41
	v_mul_f32_e32 v42, 0x42000000, v42
	v_mul_f32_e32 v43, 0x42000000, v43
	v_mul_f32_e32 v44, 0x42000000, v44
	v_mul_f32_e32 v45, 0x42000000, v45
	v_mul_f32_e32 v46, 0x42000000, v46
	v_mul_f32_e32 v47, 0x42000000, v47
	v_mul_f32_e32 v48, 0x42000000, v48
	v_mul_f32_e32 v49, 0x42000000, v49
	v_cvt_pk_fp8_f32 v154, v34, v35
	v_cvt_pk_fp8_f32 v155, v38, v39
	v_cvt_pk_fp8_f32 v156, v42, v43
	v_cvt_pk_fp8_f32 v157, v46, v47
	v_cvt_pk_fp8_f32 v154, v36, v37 op_sel:[0,0,1]
	v_cvt_pk_fp8_f32 v155, v40, v41 op_sel:[0,0,1]
	v_cvt_pk_fp8_f32 v156, v44, v45 op_sel:[0,0,1]
	v_cvt_pk_fp8_f32 v157, v48, v49 op_sel:[0,0,1]
	s_waitcnt vmcnt(32)
	v_mul_f32_e32 v50, 0x42000000, v50
	v_mul_f32_e32 v51, 0x42000000, v51
	v_mul_f32_e32 v52, 0x42000000, v52
	v_mul_f32_e32 v53, 0x42000000, v53
	v_mul_f32_e32 v54, 0x42000000, v54
	v_mul_f32_e32 v55, 0x42000000, v55
	v_mul_f32_e32 v56, 0x42000000, v56
	v_mul_f32_e32 v57, 0x42000000, v57
	v_mul_f32_e32 v58, 0x42000000, v58
	v_mul_f32_e32 v59, 0x42000000, v59
	v_mul_f32_e32 v60, 0x42000000, v60
	v_mul_f32_e32 v61, 0x42000000, v61
	v_mul_f32_e32 v62, 0x42000000, v62
	v_mul_f32_e32 v63, 0x42000000, v63
	v_mul_f32_e32 v64, 0x42000000, v64
	v_mul_f32_e32 v65, 0x42000000, v65
	v_cvt_pk_fp8_f32 v158, v50, v51
	v_cvt_pk_fp8_f32 v159, v54, v55
	v_cvt_pk_fp8_f32 v160, v58, v59
	v_cvt_pk_fp8_f32 v161, v62, v63
	v_cvt_pk_fp8_f32 v158, v52, v53 op_sel:[0,0,1]
	v_cvt_pk_fp8_f32 v159, v56, v57 op_sel:[0,0,1]
	v_cvt_pk_fp8_f32 v160, v60, v61 op_sel:[0,0,1]
	v_cvt_pk_fp8_f32 v161, v64, v65 op_sel:[0,0,1]
	s_waitcnt vmcnt(16)
	v_mul_f32_e32 v66, 0x42000000, v66
	v_mul_f32_e32 v67, 0x42000000, v67
	v_mul_f32_e32 v68, 0x42000000, v68
	v_mul_f32_e32 v69, 0x42000000, v69
	v_mul_f32_e32 v70, 0x42000000, v70
	v_mul_f32_e32 v71, 0x42000000, v71
	v_mul_f32_e32 v72, 0x42000000, v72
	v_mul_f32_e32 v73, 0x42000000, v73
	v_mul_f32_e32 v74, 0x42000000, v74
	v_mul_f32_e32 v75, 0x42000000, v75
	v_mul_f32_e32 v76, 0x42000000, v76
	v_mul_f32_e32 v77, 0x42000000, v77
	v_mul_f32_e32 v78, 0x42000000, v78
	v_mul_f32_e32 v79, 0x42000000, v79
	v_mul_f32_e32 v80, 0x42000000, v80
	v_mul_f32_e32 v81, 0x42000000, v81
	v_cvt_pk_fp8_f32 v162, v66, v67
	v_cvt_pk_fp8_f32 v163, v70, v71
	v_cvt_pk_fp8_f32 v164, v74, v75
	v_cvt_pk_fp8_f32 v165, v78, v79
	v_cvt_pk_fp8_f32 v162, v68, v69 op_sel:[0,0,1]
	v_cvt_pk_fp8_f32 v163, v72, v73 op_sel:[0,0,1]
	v_cvt_pk_fp8_f32 v164, v76, v77 op_sel:[0,0,1]
	v_cvt_pk_fp8_f32 v165, v80, v81 op_sel:[0,0,1]
	s_waitcnt vmcnt(0)
	v_mul_f32_e32 v82, 0x42000000, v82
	v_mul_f32_e32 v83, 0x42000000, v83
	v_mul_f32_e32 v84, 0x42000000, v84
	v_mul_f32_e32 v85, 0x42000000, v85
	v_mul_f32_e32 v86, 0x42000000, v86
	v_mul_f32_e32 v87, 0x42000000, v87
	v_mul_f32_e32 v88, 0x42000000, v88
	v_mul_f32_e32 v89, 0x42000000, v89
	v_mul_f32_e32 v90, 0x42000000, v90
	v_mul_f32_e32 v91, 0x42000000, v91
	v_mul_f32_e32 v92, 0x42000000, v92
	v_mul_f32_e32 v93, 0x42000000, v93
	v_mul_f32_e32 v94, 0x42000000, v94
	v_mul_f32_e32 v95, 0x42000000, v95
	v_mul_f32_e32 v96, 0x42000000, v96
	v_mul_f32_e32 v97, 0x42000000, v97
	v_cvt_pk_fp8_f32 v166, v82, v83
	v_cvt_pk_fp8_f32 v167, v86, v87
	v_cvt_pk_fp8_f32 v168, v90, v91
	v_cvt_pk_fp8_f32 v169, v94, v95
	v_cvt_pk_fp8_f32 v166, v84, v85 op_sel:[0,0,1]
	v_cvt_pk_fp8_f32 v167, v88, v89 op_sel:[0,0,1]
	v_cvt_pk_fp8_f32 v168, v92, v93 op_sel:[0,0,1]
	v_cvt_pk_fp8_f32 v169, v96, v97 op_sel:[0,0,1]
	s_mov_b32 vcc_lo, 0xaaaaaaaa
	s_mov_b32 vcc_hi, 0xaaaaaaaa
	s_nop 1
	v_cndmask_b32_dpp v170, v154, v158, vcc quad_perm:[1,0,3,2] row_mask:0xf bank_mask:0xf
	v_cndmask_b32_dpp v174, v162, v166, vcc quad_perm:[1,0,3,2] row_mask:0xf bank_mask:0xf
	v_cndmask_b32_dpp v171, v155, v159, vcc quad_perm:[1,0,3,2] row_mask:0xf bank_mask:0xf
	v_cndmask_b32_dpp v175, v163, v167, vcc quad_perm:[1,0,3,2] row_mask:0xf bank_mask:0xf
	v_cndmask_b32_dpp v172, v156, v160, vcc quad_perm:[1,0,3,2] row_mask:0xf bank_mask:0xf
	v_cndmask_b32_dpp v176, v164, v168, vcc quad_perm:[1,0,3,2] row_mask:0xf bank_mask:0xf
	v_cndmask_b32_dpp v173, v157, v161, vcc quad_perm:[1,0,3,2] row_mask:0xf bank_mask:0xf
	v_cndmask_b32_dpp v177, v165, v169, vcc quad_perm:[1,0,3,2] row_mask:0xf bank_mask:0xf
	s_mov_b32 vcc_lo, 0x55555555
	s_mov_b32 vcc_hi, 0x55555555
	s_nop 1
	v_cndmask_b32_dpp v154, v158, v154, vcc quad_perm:[1,0,3,2] row_mask:0xf bank_mask:0xf
	v_cndmask_b32_dpp v162, v166, v162, vcc quad_perm:[1,0,3,2] row_mask:0xf bank_mask:0xf
	v_cndmask_b32_dpp v155, v159, v155, vcc quad_perm:[1,0,3,2] row_mask:0xf bank_mask:0xf
	v_cndmask_b32_dpp v163, v167, v163, vcc quad_perm:[1,0,3,2] row_mask:0xf bank_mask:0xf
	v_cndmask_b32_dpp v156, v160, v156, vcc quad_perm:[1,0,3,2] row_mask:0xf bank_mask:0xf
	v_cndmask_b32_dpp v164, v168, v164, vcc quad_perm:[1,0,3,2] row_mask:0xf bank_mask:0xf
	v_cndmask_b32_dpp v157, v161, v157, vcc quad_perm:[1,0,3,2] row_mask:0xf bank_mask:0xf
	v_cndmask_b32_dpp v165, v169, v165, vcc quad_perm:[1,0,3,2] row_mask:0xf bank_mask:0xf
	s_mov_b32 vcc_lo, 0xcccccccc
	s_mov_b32 vcc_hi, 0xcccccccc
	s_nop 1
	v_cndmask_b32_dpp v158, v154, v162, vcc quad_perm:[2,3,0,1] row_mask:0xf bank_mask:0xf
	v_cndmask_b32_dpp v166, v170, v174, vcc quad_perm:[2,3,0,1] row_mask:0xf bank_mask:0xf
	v_cndmask_b32_dpp v159, v155, v163, vcc quad_perm:[2,3,0,1] row_mask:0xf bank_mask:0xf
	v_cndmask_b32_dpp v167, v171, v175, vcc quad_perm:[2,3,0,1] row_mask:0xf bank_mask:0xf
	v_cndmask_b32_dpp v160, v156, v164, vcc quad_perm:[2,3,0,1] row_mask:0xf bank_mask:0xf
	v_cndmask_b32_dpp v168, v172, v176, vcc quad_perm:[2,3,0,1] row_mask:0xf bank_mask:0xf
	v_cndmask_b32_dpp v161, v157, v165, vcc quad_perm:[2,3,0,1] row_mask:0xf bank_mask:0xf
	v_cndmask_b32_dpp v169, v173, v177, vcc quad_perm:[2,3,0,1] row_mask:0xf bank_mask:0xf
	s_mov_b32 vcc_lo, 0x33333333
	s_mov_b32 vcc_hi, 0x33333333
	s_nop 1
	v_cndmask_b32_dpp v154, v162, v154, vcc quad_perm:[2,3,0,1] row_mask:0xf bank_mask:0xf
	v_cndmask_b32_dpp v170, v174, v170, vcc quad_perm:[2,3,0,1] row_mask:0xf bank_mask:0xf
	v_cndmask_b32_dpp v155, v163, v155, vcc quad_perm:[2,3,0,1] row_mask:0xf bank_mask:0xf
	v_cndmask_b32_dpp v171, v175, v171, vcc quad_perm:[2,3,0,1] row_mask:0xf bank_mask:0xf
	v_cndmask_b32_dpp v156, v164, v156, vcc quad_perm:[2,3,0,1] row_mask:0xf bank_mask:0xf
	v_cndmask_b32_dpp v172, v176, v172, vcc quad_perm:[2,3,0,1] row_mask:0xf bank_mask:0xf
	v_cndmask_b32_dpp v157, v165, v157, vcc quad_perm:[2,3,0,1] row_mask:0xf bank_mask:0xf
	v_cndmask_b32_dpp v173, v177, v173, vcc quad_perm:[2,3,0,1] row_mask:0xf bank_mask:0xf
	global_store_dwordx4 v179, v[154:157], s[82:83]
	global_store_dwordx4 v180, v[170:173], s[82:83]
	global_store_dwordx4 v181, v[158:161], s[82:83]
	global_store_dwordx4 v190, v[166:169], s[82:83]
	v_readlane_b32 s2, v239, 0
	s_lshr_b32 s2, s2, 6
	s_add_i32 s2, s2, 6
	s_cmp_gt_u32 s2, 13
	s_cbranch_scc1 .Lhw_seam5_done
	s_add_i32 s2, s2, 70
	s_mul_i32 s2, s2, s74
	v_readlane_b32 s9, v239, 23
	s_lshr_b32 s9, s9, 3
	s_add_i32 s2, s2, s9
	s_cmp_gt_u32 s2, 24575
	s_cbranch_scc1 .Lhw_seam5_done
	v_mbcnt_lo_u32_b32 v178, -1, 0
	v_mbcnt_hi_u32_b32 v178, -1, v178
	v_and_b32_e32 v179, 60, v178
	v_lshlrev_b32_e32 v179, 10, v179
	v_and_b32_e32 v180, 3, v178
	v_lshl_or_b32 v179, v180, 4, v179
	v_add_u32_e32 v180, 0x400, v179
	v_add_u32_e32 v181, 0x800, v179
	v_add_u32_e32 v190, 0xc00, v179
	v_lshlrev_b32_e32 v178, 2, v178
	s_cmp_lt_u32 s2, 16384
	s_cbranch_scc0 .Lhw_dn_s5_1
	s_lshr_b32 s9, s2, 9
	s_bfe_u32 s32, s2, 0x40005
	s_and_b32 s53, s2, 31
	s_lshl_b32 s69, s9, 23
	s_lshl_b32 s100, s32, 19
	s_add_i32 s69, s69, s100
	s_lshl_b32 s100, s53, 8
	s_add_i32 s69, s69, s100
	s_lshl_b32 s98, s9, 11
	s_bfe_u32 s100, s53, 0x30001
	s_lshl_b32 s100, s100, 8
	s_add_i32 s98, s98, s100
	s_lshr_b32 s100, s53, 4
	s_lshl_b32 s100, s100, 7
	s_add_i32 s98, s98, s100
	s_and_b32 s100, s53, 1
	s_lshl_b32 s100, s100, 6
	s_add_i32 s98, s98, s100
	s_lshl_b32 s98, s98, 10
	s_lshl_b32 s100, s32, 6
	s_add_i32 s98, s98, s100
	s_add_i32 s98, s98, 0x2000000
	v_readlane_b32 s82, v239, 11
	v_readlane_b32 s83, v239, 12
	s_movk_i32 s89, 8192
	s_branch .Lhw_go_s5_1

.Lhw_go_s6_0:
	s_add_u32 s100, s82, s69
	s_addc_u32 s101, s83, 0
	v_readlane_b32 s82, v239, 44
	v_readlane_b32 s83, v239, 45
	s_add_u32 s82, s82, s98
	s_addc_u32 s83, s83, 0
	global_load_dword v34, v178, s[100:101] nt
	s_add_u32 s100, s100, s89
	s_addc_u32 s101, s101, 0
	global_load_dword v35, v178, s[100:101] nt
	s_add_u32 s100, s100, s89
	s_addc_u32 s101, s101, 0
	global_load_dword v36, v178, s[100:101] nt
	s_add_u32 s100, s100, s89
	s_addc_u32 s101, s101, 0
	global_load_dword v37, v178, s[100:101] nt
	s_add_u32 s100, s100, s89
	s_addc_u32 s101, s101, 0
	global_load_dword v38, v178, s[100:101] nt
	s_add_u32 s100, s100, s89
	s_addc_u32 s101, s101, 0
	global_load_dword v39, v178, s[100:101] nt
	s_add_u32 s100, s100, s89
	s_addc_u32 s101, s101, 0
	global_load_dword v40, v178, s[100:101] nt
	s_add_u32 s100, s100, s89
	s_addc_u32 s101, s101, 0
	global_load_dword v41, v178, s[100:101] nt
	s_add_u32 s100, s100, s89
	s_addc_u32 s101, s101, 0
	global_load_dword v42, v178, s[100:101] nt
	s_add_u32 s100, s100, s89
	s_addc_u32 s101, s101, 0
	global_load_dword v43, v178, s[100:101] nt
	s_add_u32 s100, s100, s89
	s_addc_u32 s101, s101, 0
	global_load_dword v44, v178, s[100:101] nt
	s_add_u32 s100, s100, s89
	s_addc_u32 s101, s101, 0
	global_load_dword v45, v178, s[100:101] nt
	s_add_u32 s100, s100, s89
	s_addc_u32 s101, s101, 0
	global_load_dword v46, v178, s[100:101] nt
	s_add_u32 s100, s100, s89
	s_addc_u32 s101, s101, 0
	global_load_dword v47, v178, s[100:101] nt
	s_add_u32 s100, s100, s89
	s_addc_u32 s101, s101, 0
	global_load_dword v48, v178, s[100:101] nt
	s_add_u32 s100, s100, s89
	s_addc_u32 s101, s101, 0
	global_load_dword v49, v178, s[100:101] nt
	s_add_u32 s100, s100, s89
	s_addc_u32 s101, s101, 0
	global_load_dword v50, v178, s[100:101] nt
	s_add_u32 s100, s100, s89
	s_addc_u32 s101, s101, 0
	global_load_dword v51, v178, s[100:101] nt
	s_add_u32 s100, s100, s89
	s_addc_u32 s101, s101, 0
	global_load_dword v52, v178, s[100:101] nt
	s_add_u32 s100, s100, s89
	s_addc_u32 s101, s101, 0
	global_load_dword v53, v178, s[100:101] nt
	s_add_u32 s100, s100, s89
	s_addc_u32 s101, s101, 0
	global_load_dword v54, v178, s[100:101] nt
	s_add_u32 s100, s100, s89
	s_addc_u32 s101, s101, 0
	global_load_dword v55, v178, s[100:101] nt
	s_add_u32 s100, s100, s89
	s_addc_u32 s101, s101, 0
	global_load_dword v56, v178, s[100:101] nt
	s_add_u32 s100, s100, s89
	s_addc_u32 s101, s101, 0
	global_load_dword v57, v178, s[100:101] nt
	s_add_u32 s100, s100, s89
	s_addc_u32 s101, s101, 0
	global_load_dword v58, v178, s[100:101] nt
	s_add_u32 s100, s100, s89
	s_addc_u32 s101, s101, 0
	global_load_dword v59, v178, s[100:101] nt
	s_add_u32 s100, s100, s89
	s_addc_u32 s101, s101, 0
	global_load_dword v60, v178, s[100:101] nt
	s_add_u32 s100, s100, s89
	s_addc_u32 s101, s101, 0
	global_load_dword v61, v178, s[100:101] nt
	s_add_u32 s100, s100, s89
	s_addc_u32 s101, s101, 0
	global_load_dword v62, v178, s[100:101] nt
	s_add_u32 s100, s100, s89
	s_addc_u32 s101, s101, 0
	global_load_dword v63, v178, s[100:101] nt
	s_add_u32 s100, s100, s89
	s_addc_u32 s101, s101, 0
	global_load_dword v64, v178, s[100:101] nt
	s_add_u32 s100, s100, s89
	s_addc_u32 s101, s101, 0
	global_load_dword v65, v178, s[100:101] nt
	s_add_u32 s100, s100, s89
	s_addc_u32 s101, s101, 0
	global_load_dword v66, v178, s[100:101] nt
	s_add_u32 s100, s100, s89
	s_addc_u32 s101, s101, 0
	global_load_dword v67, v178, s[100:101] nt
	s_add_u32 s100, s100, s89
	s_addc_u32 s101, s101, 0
	global_load_dword v68, v178, s[100:101] nt
	s_add_u32 s100, s100, s89
	s_addc_u32 s101, s101, 0
	global_load_dword v69, v178, s[100:101] nt
	s_add_u32 s100, s100, s89
	s_addc_u32 s101, s101, 0
	global_load_dword v70, v178, s[100:101] nt
	s_add_u32 s100, s100, s89
	s_addc_u32 s101, s101, 0
	global_load_dword v71, v178, s[100:101] nt
	s_add_u32 s100, s100, s89
	s_addc_u32 s101, s101, 0
	global_load_dword v72, v178, s[100:101] nt
	s_add_u32 s100, s100, s89
	s_addc_u32 s101, s101, 0
	global_load_dword v73, v178, s[100:101] nt
	s_add_u32 s100, s100, s89
	s_addc_u32 s101, s101, 0
	global_load_dword v74, v178, s[100:101] nt
	s_add_u32 s100, s100, s89
	s_addc_u32 s101, s101, 0
	global_load_dword v75, v178, s[100:101] nt
	s_add_u32 s100, s100, s89
	s_addc_u32 s101, s101, 0
	global_load_dword v76, v178, s[100:101] nt
	s_add_u32 s100, s100, s89
	s_addc_u32 s101, s101, 0
	global_load_dword v77, v178, s[100:101] nt
	s_add_u32 s100, s100, s89
	s_addc_u32 s101, s101, 0
	global_load_dword v78, v178, s[100:101] nt
	s_add_u32 s100, s100, s89
	s_addc_u32 s101, s101, 0
	global_load_dword v79, v178, s[100:101] nt
	s_add_u32 s100, s100, s89
	s_addc_u32 s101, s101, 0
	global_load_dword v80, v178, s[100:101] nt
	s_add_u32 s100, s100, s89
	s_addc_u32 s101, s101, 0
	global_load_dword v81, v178, s[100:101] nt
	s_add_u32 s100, s100, s89
	s_addc_u32 s101, s101, 0
	global_load_dword v82, v178, s[100:101] nt
	s_add_u32 s100, s100, s89
	s_addc_u32 s101, s101, 0
	global_load_dword v83, v178, s[100:101] nt
	s_add_u32 s100, s100, s89
	s_addc_u32 s101, s101, 0
	global_load_dword v84, v178, s[100:101] nt
	s_add_u32 s100, s100, s89
	s_addc_u32 s101, s101, 0
	global_load_dword v85, v178, s[100:101] nt
	s_add_u32 s100, s100, s89
	s_addc_u32 s101, s101, 0
	global_load_dword v86, v178, s[100:101] nt
	s_add_u32 s100, s100, s89
	s_addc_u32 s101, s101, 0
	global_load_dword v87, v178, s[100:101] nt
	s_add_u32 s100, s100, s89
	s_addc_u32 s101, s101, 0
	global_load_dword v88, v178, s[100:101] nt
	s_add_u32 s100, s100, s89
	s_addc_u32 s101, s101, 0
	global_load_dword v89, v178, s[100:101] nt
	s_add_u32 s100, s100, s89
	s_addc_u32 s101, s101, 0
	global_load_dword v90, v178, s[100:101] nt
	s_add_u32 s100, s100, s89
	s_addc_u32 s101, s101, 0
	global_load_dword v91, v178, s[100:101] nt
	s_add_u32 s100, s100, s89
	s_addc_u32 s101, s101, 0
	global_load_dword v92, v178, s[100:101] nt
	s_add_u32 s100, s100, s89
	s_addc_u32 s101, s101, 0
	global_load_dword v93, v178, s[100:101] nt
	s_add_u32 s100, s100, s89
	s_addc_u32 s101, s101, 0
	global_load_dword v94, v178, s[100:101] nt
	s_add_u32 s100, s100, s89
	s_addc_u32 s101, s101, 0
	global_load_dword v95, v178, s[100:101] nt
	s_add_u32 s100, s100, s89
	s_addc_u32 s101, s101, 0
	global_load_dword v96, v178, s[100:101] nt
	s_add_u32 s100, s100, s89
	s_addc_u32 s101, s101, 0
	global_load_dword v97, v178, s[100:101] nt
	s_add_u32 s100, s100, s89
	s_addc_u32 s101, s101, 0
	s_waitcnt vmcnt(48)
	v_mul_f32_e32 v34, 0x42000000, v34
	v_mul_f32_e32 v35, 0x42000000, v35
	v_mul_f32_e32 v36, 0x42000000, v36
	v_mul_f32_e32 v37, 0x42000000, v37
	v_mul_f32_e32 v38, 0x42000000, v38
	v_mul_f32_e32 v39, 0x42000000, v39
	v_mul_f32_e32 v40, 0x42000000, v40
	v_mul_f32_e32 v41, 0x42000000, v41
	v_mul_f32_e32 v42, 0x42000000, v42
	v_mul_f32_e32 v43, 0x42000000, v43
	v_mul_f32_e32 v44, 0x42000000, v44
	v_mul_f32_e32 v45, 0x42000000, v45
	v_mul_f32_e32 v46, 0x42000000, v46
	v_mul_f32_e32 v47, 0x42000000, v47
	v_mul_f32_e32 v48, 0x42000000, v48
	v_mul_f32_e32 v49, 0x42000000, v49
	v_cvt_pk_fp8_f32 v154, v34, v35
	v_cvt_pk_fp8_f32 v155, v38, v39
	v_cvt_pk_fp8_f32 v156, v42, v43
	v_cvt_pk_fp8_f32 v157, v46, v47
	v_cvt_pk_fp8_f32 v154, v36, v37 op_sel:[0,0,1]
	v_cvt_pk_fp8_f32 v155, v40, v41 op_sel:[0,0,1]
	v_cvt_pk_fp8_f32 v156, v44, v45 op_sel:[0,0,1]
	v_cvt_pk_fp8_f32 v157, v48, v49 op_sel:[0,0,1]
	s_waitcnt vmcnt(32)
	v_mul_f32_e32 v50, 0x42000000, v50
	v_mul_f32_e32 v51, 0x42000000, v51
	v_mul_f32_e32 v52, 0x42000000, v52
	v_mul_f32_e32 v53, 0x42000000, v53
	v_mul_f32_e32 v54, 0x42000000, v54
	v_mul_f32_e32 v55, 0x42000000, v55
	v_mul_f32_e32 v56, 0x42000000, v56
	v_mul_f32_e32 v57, 0x42000000, v57
	v_mul_f32_e32 v58, 0x42000000, v58
	v_mul_f32_e32 v59, 0x42000000, v59
	v_mul_f32_e32 v60, 0x42000000, v60
	v_mul_f32_e32 v61, 0x42000000, v61
	v_mul_f32_e32 v62, 0x42000000, v62
	v_mul_f32_e32 v63, 0x42000000, v63
	v_mul_f32_e32 v64, 0x42000000, v64
	v_mul_f32_e32 v65, 0x42000000, v65
	v_cvt_pk_fp8_f32 v158, v50, v51
	v_cvt_pk_fp8_f32 v159, v54, v55
	v_cvt_pk_fp8_f32 v160, v58, v59
	v_cvt_pk_fp8_f32 v161, v62, v63
	v_cvt_pk_fp8_f32 v158, v52, v53 op_sel:[0,0,1]
	v_cvt_pk_fp8_f32 v159, v56, v57 op_sel:[0,0,1]
	v_cvt_pk_fp8_f32 v160, v60, v61 op_sel:[0,0,1]
	v_cvt_pk_fp8_f32 v161, v64, v65 op_sel:[0,0,1]
	s_waitcnt vmcnt(16)
	v_mul_f32_e32 v66, 0x42000000, v66
	v_mul_f32_e32 v67, 0x42000000, v67
	v_mul_f32_e32 v68, 0x42000000, v68
	v_mul_f32_e32 v69, 0x42000000, v69
	v_mul_f32_e32 v70, 0x42000000, v70
	v_mul_f32_e32 v71, 0x42000000, v71
	v_mul_f32_e32 v72, 0x42000000, v72
	v_mul_f32_e32 v73, 0x42000000, v73
	v_mul_f32_e32 v74, 0x42000000, v74
	v_mul_f32_e32 v75, 0x42000000, v75
	v_mul_f32_e32 v76, 0x42000000, v76
	v_mul_f32_e32 v77, 0x42000000, v77
	v_mul_f32_e32 v78, 0x42000000, v78
	v_mul_f32_e32 v79, 0x42000000, v79
	v_mul_f32_e32 v80, 0x42000000, v80
	v_mul_f32_e32 v81, 0x42000000, v81
	v_cvt_pk_fp8_f32 v162, v66, v67
	v_cvt_pk_fp8_f32 v163, v70, v71
	v_cvt_pk_fp8_f32 v164, v74, v75
	v_cvt_pk_fp8_f32 v165, v78, v79
	v_cvt_pk_fp8_f32 v162, v68, v69 op_sel:[0,0,1]
	v_cvt_pk_fp8_f32 v163, v72, v73 op_sel:[0,0,1]
	v_cvt_pk_fp8_f32 v164, v76, v77 op_sel:[0,0,1]
	v_cvt_pk_fp8_f32 v165, v80, v81 op_sel:[0,0,1]
	s_waitcnt vmcnt(0)
	v_mul_f32_e32 v82, 0x42000000, v82
	v_mul_f32_e32 v83, 0x42000000, v83
	v_mul_f32_e32 v84, 0x42000000, v84
	v_mul_f32_e32 v85, 0x42000000, v85
	v_mul_f32_e32 v86, 0x42000000, v86
	v_mul_f32_e32 v87, 0x42000000, v87
	v_mul_f32_e32 v88, 0x42000000, v88
	v_mul_f32_e32 v89, 0x42000000, v89
	v_mul_f32_e32 v90, 0x42000000, v90
	v_mul_f32_e32 v91, 0x42000000, v91
	v_mul_f32_e32 v92, 0x42000000, v92
	v_mul_f32_e32 v93, 0x42000000, v93
	v_mul_f32_e32 v94, 0x42000000, v94
	v_mul_f32_e32 v95, 0x42000000, v95
	v_mul_f32_e32 v96, 0x42000000, v96
	v_mul_f32_e32 v97, 0x42000000, v97
	v_cvt_pk_fp8_f32 v166, v82, v83
	v_cvt_pk_fp8_f32 v167, v86, v87
	v_cvt_pk_fp8_f32 v168, v90, v91
	v_cvt_pk_fp8_f32 v169, v94, v95
	v_cvt_pk_fp8_f32 v166, v84, v85 op_sel:[0,0,1]
	v_cvt_pk_fp8_f32 v167, v88, v89 op_sel:[0,0,1]
	v_cvt_pk_fp8_f32 v168, v92, v93 op_sel:[0,0,1]
	v_cvt_pk_fp8_f32 v169, v96, v97 op_sel:[0,0,1]
	s_mov_b32 vcc_lo, 0xaaaaaaaa
	s_mov_b32 vcc_hi, 0xaaaaaaaa
	s_nop 1
	v_cndmask_b32_dpp v170, v154, v158, vcc quad_perm:[1,0,3,2] row_mask:0xf bank_mask:0xf
	v_cndmask_b32_dpp v174, v162, v166, vcc quad_perm:[1,0,3,2] row_mask:0xf bank_mask:0xf
	v_cndmask_b32_dpp v171, v155, v159, vcc quad_perm:[1,0,3,2] row_mask:0xf bank_mask:0xf
	v_cndmask_b32_dpp v175, v163, v167, vcc quad_perm:[1,0,3,2] row_mask:0xf bank_mask:0xf
	v_cndmask_b32_dpp v172, v156, v160, vcc quad_perm:[1,0,3,2] row_mask:0xf bank_mask:0xf
	v_cndmask_b32_dpp v176, v164, v168, vcc quad_perm:[1,0,3,2] row_mask:0xf bank_mask:0xf
	v_cndmask_b32_dpp v173, v157, v161, vcc quad_perm:[1,0,3,2] row_mask:0xf bank_mask:0xf
	v_cndmask_b32_dpp v177, v165, v169, vcc quad_perm:[1,0,3,2] row_mask:0xf bank_mask:0xf
	s_mov_b32 vcc_lo, 0x55555555
	s_mov_b32 vcc_hi, 0x55555555
	s_nop 1
	v_cndmask_b32_dpp v154, v158, v154, vcc quad_perm:[1,0,3,2] row_mask:0xf bank_mask:0xf
	v_cndmask_b32_dpp v162, v166, v162, vcc quad_perm:[1,0,3,2] row_mask:0xf bank_mask:0xf
	v_cndmask_b32_dpp v155, v159, v155, vcc quad_perm:[1,0,3,2] row_mask:0xf bank_mask:0xf
	v_cndmask_b32_dpp v163, v167, v163, vcc quad_perm:[1,0,3,2] row_mask:0xf bank_mask:0xf
	v_cndmask_b32_dpp v156, v160, v156, vcc quad_perm:[1,0,3,2] row_mask:0xf bank_mask:0xf
	v_cndmask_b32_dpp v164, v168, v164, vcc quad_perm:[1,0,3,2] row_mask:0xf bank_mask:0xf
	v_cndmask_b32_dpp v157, v161, v157, vcc quad_perm:[1,0,3,2] row_mask:0xf bank_mask:0xf
	v_cndmask_b32_dpp v165, v169, v165, vcc quad_perm:[1,0,3,2] row_mask:0xf bank_mask:0xf
	s_mov_b32 vcc_lo, 0xcccccccc
	s_mov_b32 vcc_hi, 0xcccccccc
	s_nop 1
	v_cndmask_b32_dpp v158, v154, v162, vcc quad_perm:[2,3,0,1] row_mask:0xf bank_mask:0xf
	v_cndmask_b32_dpp v166, v170, v174, vcc quad_perm:[2,3,0,1] row_mask:0xf bank_mask:0xf
	v_cndmask_b32_dpp v159, v155, v163, vcc quad_perm:[2,3,0,1] row_mask:0xf bank_mask:0xf
	v_cndmask_b32_dpp v167, v171, v175, vcc quad_perm:[2,3,0,1] row_mask:0xf bank_mask:0xf
	v_cndmask_b32_dpp v160, v156, v164, vcc quad_perm:[2,3,0,1] row_mask:0xf bank_mask:0xf
	v_cndmask_b32_dpp v168, v172, v176, vcc quad_perm:[2,3,0,1] row_mask:0xf bank_mask:0xf
	v_cndmask_b32_dpp v161, v157, v165, vcc quad_perm:[2,3,0,1] row_mask:0xf bank_mask:0xf
	v_cndmask_b32_dpp v169, v173, v177, vcc quad_perm:[2,3,0,1] row_mask:0xf bank_mask:0xf
	s_mov_b32 vcc_lo, 0x33333333
	s_mov_b32 vcc_hi, 0x33333333
	s_nop 1
	v_cndmask_b32_dpp v154, v162, v154, vcc quad_perm:[2,3,0,1] row_mask:0xf bank_mask:0xf
	v_cndmask_b32_dpp v170, v174, v170, vcc quad_perm:[2,3,0,1] row_mask:0xf bank_mask:0xf
	v_cndmask_b32_dpp v155, v163, v155, vcc quad_perm:[2,3,0,1] row_mask:0xf bank_mask:0xf
	v_cndmask_b32_dpp v171, v175, v171, vcc quad_perm:[2,3,0,1] row_mask:0xf bank_mask:0xf
	v_cndmask_b32_dpp v156, v164, v156, vcc quad_perm:[2,3,0,1] row_mask:0xf bank_mask:0xf
	v_cndmask_b32_dpp v172, v176, v172, vcc quad_perm:[2,3,0,1] row_mask:0xf bank_mask:0xf
	v_cndmask_b32_dpp v157, v165, v157, vcc quad_perm:[2,3,0,1] row_mask:0xf bank_mask:0xf
	v_cndmask_b32_dpp v173, v177, v173, vcc quad_perm:[2,3,0,1] row_mask:0xf bank_mask:0xf
	global_store_dwordx4 v179, v[154:157], s[82:83]
	global_store_dwordx4 v180, v[170:173], s[82:83]
	global_store_dwordx4 v181, v[158:161], s[82:83]
	global_store_dwordx4 v190, v[166:169], s[82:83]
	v_readlane_b32 s2, v239, 0
	s_lshr_b32 s2, s2, 6
	s_add_i32 s2, s2, 6
	s_cmp_gt_u32 s2, 11
	s_cbranch_scc1 .Lhw_seam6_done
	s_add_i32 s2, s2, 84
	s_mul_i32 s2, s2, s74
	v_readlane_b32 s9, v239, 23
	s_lshr_b32 s9, s9, 3
	s_add_i32 s2, s2, s9
	s_cmp_gt_u32 s2, 24575
	s_cbranch_scc1 .Lhw_seam6_done
	v_mbcnt_lo_u32_b32 v178, -1, 0
	v_mbcnt_hi_u32_b32 v178, -1, v178
	v_and_b32_e32 v179, 60, v178
	v_lshlrev_b32_e32 v179, 10, v179
	v_and_b32_e32 v180, 3, v178
	v_lshl_or_b32 v179, v180, 4, v179
	v_add_u32_e32 v180, 0x400, v179
	v_add_u32_e32 v181, 0x800, v179
	v_add_u32_e32 v190, 0xc00, v179
	v_lshlrev_b32_e32 v178, 2, v178
	s_cmp_lt_u32 s2, 16384
	s_cbranch_scc0 .Lhw_dn_s6_1
	s_lshr_b32 s9, s2, 9
	s_bfe_u32 s32, s2, 0x40005
	s_and_b32 s53, s2, 31
	s_lshl_b32 s69, s9, 23
	s_lshl_b32 s100, s32, 19
	s_add_i32 s69, s69, s100
	s_lshl_b32 s100, s53, 8
	s_add_i32 s69, s69, s100
	s_lshl_b32 s98, s9, 11
	s_bfe_u32 s100, s53, 0x30001
	s_lshl_b32 s100, s100, 8
	s_add_i32 s98, s98, s100
	s_lshr_b32 s100, s53, 4
	s_lshl_b32 s100, s100, 7
	s_add_i32 s98, s98, s100
	s_and_b32 s100, s53, 1
	s_lshl_b32 s100, s100, 6
	s_add_i32 s98, s98, s100
	s_lshl_b32 s98, s98, 10
	s_lshl_b32 s100, s32, 6
	s_add_i32 s98, s98, s100
	s_add_i32 s98, s98, 0x2000000
	v_readlane_b32 s82, v239, 11
	v_readlane_b32 s83, v239, 12
	s_movk_i32 s89, 8192
	s_branch .Lhw_go_s6_1
